# GEMM epilogue stores non-temporal (nt)
# baseline (speedup 1.0000x reference)
.LBB0_382:
	s_and_b32 s22, s56, 0x7ffffffc
	s_cmp_eq_u32 s22, 24
	s_cselect_b64 vcc, -1, 0
	s_cmp_lg_u32 s22, 12
	v_cndmask_b32_e32 v1, 1.0, v163, vcc
	s_cselect_b64 vcc, -1, 0
	s_cmp_gt_i32 s56, 3
	v_cndmask_b32_e32 v1, v164, v1, vcc
	s_cselect_b64 vcc, -1, 0
	v_lshl_or_b32 v146, s56, 8, v157
	v_cndmask_b32_e32 v142, v165, v1, vcc
	v_lshl_add_u32 v1, s55, 8, v156
	v_ashrrev_i32_e32 v147, 31, v146
	v_mov_b64_e32 v[144:145], s[88:89]
	v_mad_i64_i32 v[166:167], s[22:23], v1, s48, v[144:145]
	v_lshlrev_b64 v[146:147], 1, v[146:147]
	v_lshl_add_u64 v[166:167], v[166:167], 0, v[146:147]
	v_pk_mul_f32 v[128:129], v[142:143], v[128:129] op_sel_hi:[0,1]
	v_pk_mul_f32 v[126:127], v[142:143], v[126:127] op_sel_hi:[0,1]
	v_pk_mul_f32 v[168:169], v[142:143], v[124:125] op_sel_hi:[0,1]
	v_pk_mul_f32 v[124:125], v[142:143], v[122:123] op_sel_hi:[0,1]
	v_cvt_pk_bf16_f32 v122, v126, v127
	v_cvt_pk_bf16_f32 v123, v128, v129
	v_cvt_pk_bf16_f32 v124, v124, v125
	v_cvt_pk_bf16_f32 v125, v168, v169
	global_store_dwordx4 v[166:167], v[122:125], off nt
	v_pk_mul_f32 v[118:119], v[142:143], v[118:119] op_sel_hi:[0,1]
	v_pk_mul_f32 v[120:121], v[142:143], v[120:121] op_sel_hi:[0,1]
	v_pk_mul_f32 v[122:123], v[142:143], v[112:113] op_sel_hi:[0,1]
	v_pk_mul_f32 v[112:113], v[142:143], v[110:111] op_sel_hi:[0,1]
	v_cvt_pk_bf16_f32 v110, v118, v119
	v_cvt_pk_bf16_f32 v111, v120, v121
	v_cvt_pk_bf16_f32 v112, v112, v113
	v_cvt_pk_bf16_f32 v113, v122, v123
	global_store_dwordx4 v[166:167], v[110:113], off offset:256 nt
	v_pk_mul_f32 v[114:115], v[142:143], v[114:115] op_sel_hi:[0,1]
	v_pk_mul_f32 v[102:103], v[142:143], v[102:103] op_sel_hi:[0,1]
	v_or_b32_e32 v110, 16, v1
	v_mad_i64_i32 v[110:111], s[22:23], v110, s48, v[144:145]
	v_lshl_add_u64 v[110:111], v[110:111], 0, v[146:147]
	v_pk_mul_f32 v[112:113], v[142:143], v[116:117] op_sel_hi:[0,1]
	v_pk_mul_f32 v[116:117], v[142:143], v[108:109] op_sel_hi:[0,1]
	v_pk_mul_f32 v[108:109], v[142:143], v[106:107] op_sel_hi:[0,1]
	v_cvt_pk_bf16_f32 v106, v114, v115
	v_cvt_pk_bf16_f32 v107, v112, v113
	v_cvt_pk_bf16_f32 v108, v108, v109
	v_cvt_pk_bf16_f32 v109, v116, v117
	global_store_dwordx4 v[110:111], v[106:109], off nt
	v_pk_mul_f32 v[104:105], v[142:143], v[104:105] op_sel_hi:[0,1]
	v_pk_mul_f32 v[98:99], v[142:143], v[98:99] op_sel_hi:[0,1]
	v_pk_mul_f32 v[106:107], v[142:143], v[96:97] op_sel_hi:[0,1]
	v_pk_mul_f32 v[96:97], v[142:143], v[94:95] op_sel_hi:[0,1]
	v_cvt_pk_bf16_f32 v94, v102, v103
	v_cvt_pk_bf16_f32 v95, v104, v105
	v_cvt_pk_bf16_f32 v96, v96, v97
	v_cvt_pk_bf16_f32 v97, v106, v107
	global_store_dwordx4 v[110:111], v[94:97], off offset:256 nt
	v_pk_mul_f32 v[86:87], v[142:143], v[86:87] op_sel_hi:[0,1]
	v_pk_mul_f32 v[88:89], v[142:143], v[88:89] op_sel_hi:[0,1]
	v_or_b32_e32 v94, 32, v1
	v_mad_i64_i32 v[94:95], s[22:23], v94, s48, v[144:145]
	v_lshl_add_u64 v[94:95], v[94:95], 0, v[146:147]
	v_pk_mul_f32 v[96:97], v[142:143], v[100:101] op_sel_hi:[0,1]
	v_pk_mul_f32 v[100:101], v[142:143], v[92:93] op_sel_hi:[0,1]
	v_pk_mul_f32 v[92:93], v[142:143], v[90:91] op_sel_hi:[0,1]
	v_cvt_pk_bf16_f32 v90, v98, v99
	v_cvt_pk_bf16_f32 v91, v96, v97
	v_cvt_pk_bf16_f32 v92, v92, v93
	v_cvt_pk_bf16_f32 v93, v100, v101
	global_store_dwordx4 v[94:95], v[90:93], off nt
	v_pk_mul_f32 v[82:83], v[142:143], v[82:83] op_sel_hi:[0,1]
	v_pk_mul_f32 v[70:71], v[142:143], v[70:71] op_sel_hi:[0,1]
	v_pk_mul_f32 v[90:91], v[142:143], v[80:81] op_sel_hi:[0,1]
	v_pk_mul_f32 v[80:81], v[142:143], v[78:79] op_sel_hi:[0,1]
	v_cvt_pk_bf16_f32 v78, v86, v87
	v_cvt_pk_bf16_f32 v79, v88, v89
	v_cvt_pk_bf16_f32 v80, v80, v81
	v_cvt_pk_bf16_f32 v81, v90, v91
	global_store_dwordx4 v[94:95], v[78:81], off offset:256 nt
	v_pk_mul_f32 v[72:73], v[142:143], v[72:73] op_sel_hi:[0,1]
	v_pk_mul_f32 v[64:65], v[142:143], v[64:65] op_sel_hi:[0,1]
	v_or_b32_e32 v78, 48, v1
	v_mad_i64_i32 v[78:79], s[22:23], v78, s48, v[144:145]
	v_lshl_add_u64 v[78:79], v[78:79], 0, v[146:147]
	v_pk_mul_f32 v[80:81], v[142:143], v[84:85] op_sel_hi:[0,1]
	v_pk_mul_f32 v[84:85], v[142:143], v[76:77] op_sel_hi:[0,1]
	v_pk_mul_f32 v[76:77], v[142:143], v[74:75] op_sel_hi:[0,1]
	v_cvt_pk_bf16_f32 v74, v82, v83
	v_cvt_pk_bf16_f32 v75, v80, v81
	v_cvt_pk_bf16_f32 v76, v76, v77
	v_cvt_pk_bf16_f32 v77, v84, v85
	global_store_dwordx4 v[78:79], v[74:77], off nt
	v_pk_mul_f32 v[62:63], v[142:143], v[62:63] op_sel_hi:[0,1]
	v_pk_mul_f32 v[54:55], v[142:143], v[54:55] op_sel_hi:[0,1]
	v_pk_mul_f32 v[74:75], v[142:143], v[68:69] op_sel_hi:[0,1]
	v_pk_mul_f32 v[68:69], v[142:143], v[66:67] op_sel_hi:[0,1]
	v_cvt_pk_bf16_f32 v66, v70, v71
	v_cvt_pk_bf16_f32 v67, v72, v73
	v_cvt_pk_bf16_f32 v68, v68, v69
	v_cvt_pk_bf16_f32 v69, v74, v75
	global_store_dwordx4 v[78:79], v[66:69], off offset:256 nt
	v_pk_mul_f32 v[56:57], v[142:143], v[56:57] op_sel_hi:[0,1]
	v_pk_mul_f32 v[50:51], v[142:143], v[50:51] op_sel_hi:[0,1]
	v_add_u32_e32 v66, 0x80, v1
	v_mad_i64_i32 v[66:67], s[22:23], v66, s48, v[144:145]
	v_lshl_add_u64 v[66:67], v[66:67], 0, v[146:147]
	v_pk_mul_f32 v[68:69], v[142:143], v[60:61] op_sel_hi:[0,1]
	v_pk_mul_f32 v[60:61], v[142:143], v[58:59] op_sel_hi:[0,1]
	v_cvt_pk_bf16_f32 v58, v62, v63
	v_cvt_pk_bf16_f32 v59, v64, v65
	v_cvt_pk_bf16_f32 v60, v60, v61
	v_cvt_pk_bf16_f32 v61, v68, v69
	global_store_dwordx4 v[66:67], v[58:61], off nt
	v_pk_mul_f32 v[38:39], v[142:143], v[38:39] op_sel_hi:[0,1]
	v_pk_mul_f32 v[40:41], v[142:143], v[40:41] op_sel_hi:[0,1]
	v_pk_mul_f32 v[58:59], v[142:143], v[48:49] op_sel_hi:[0,1]
	v_pk_mul_f32 v[48:49], v[142:143], v[46:47] op_sel_hi:[0,1]
	v_cvt_pk_bf16_f32 v46, v54, v55
	v_cvt_pk_bf16_f32 v47, v56, v57
	v_cvt_pk_bf16_f32 v48, v48, v49
	v_cvt_pk_bf16_f32 v49, v58, v59
	global_store_dwordx4 v[66:67], v[46:49], off offset:256 nt
	v_pk_mul_f32 v[34:35], v[142:143], v[34:35] op_sel_hi:[0,1]
	v_pk_mul_f32 v[24:25], v[142:143], v[24:25] op_sel_hi:[0,1]
	v_add_u32_e32 v46, 0x90, v1
	v_mad_i64_i32 v[46:47], s[22:23], v46, s48, v[144:145]
	v_lshl_add_u64 v[46:47], v[46:47], 0, v[146:147]
	v_pk_mul_f32 v[48:49], v[142:143], v[52:53] op_sel_hi:[0,1]
	v_pk_mul_f32 v[52:53], v[142:143], v[44:45] op_sel_hi:[0,1]
	v_pk_mul_f32 v[44:45], v[142:143], v[42:43] op_sel_hi:[0,1]
	v_cvt_pk_bf16_f32 v42, v50, v51
	v_cvt_pk_bf16_f32 v43, v48, v49
	v_cvt_pk_bf16_f32 v44, v44, v45
	v_cvt_pk_bf16_f32 v45, v52, v53
	global_store_dwordx4 v[46:47], v[42:45], off nt
	v_pk_mul_f32 v[22:23], v[142:143], v[22:23] op_sel_hi:[0,1]
	v_pk_mul_f32 v[18:19], v[142:143], v[18:19] op_sel_hi:[0,1]
	v_pk_mul_f32 v[42:43], v[142:143], v[32:33] op_sel_hi:[0,1]
	v_pk_mul_f32 v[32:33], v[142:143], v[30:31] op_sel_hi:[0,1]
	v_cvt_pk_bf16_f32 v30, v38, v39
	v_cvt_pk_bf16_f32 v31, v40, v41
	v_cvt_pk_bf16_f32 v32, v32, v33
	v_cvt_pk_bf16_f32 v33, v42, v43
	global_store_dwordx4 v[46:47], v[30:33], off offset:256 nt
	s_and_b64 vcc, exec, s[0:1]
	v_pk_mul_f32 v[8:9], v[142:143], v[8:9] op_sel_hi:[0,1]
	v_add_u32_e32 v30, 0xa0, v1
	v_mad_i64_i32 v[30:31], s[22:23], v30, s48, v[144:145]
	v_lshl_add_u64 v[30:31], v[30:31], 0, v[146:147]
	v_pk_mul_f32 v[32:33], v[142:143], v[36:37] op_sel_hi:[0,1]
	v_pk_mul_f32 v[36:37], v[142:143], v[28:29] op_sel_hi:[0,1]
	v_pk_mul_f32 v[28:29], v[142:143], v[26:27] op_sel_hi:[0,1]
	v_cvt_pk_bf16_f32 v26, v34, v35
	v_cvt_pk_bf16_f32 v27, v32, v33
	v_cvt_pk_bf16_f32 v28, v28, v29
	v_cvt_pk_bf16_f32 v29, v36, v37
	global_store_dwordx4 v[30:31], v[26:29], off nt
	v_add_u32_e32 v1, 0xb0, v1
	v_pk_mul_f32 v[6:7], v[142:143], v[6:7] op_sel_hi:[0,1]
	v_pk_mul_f32 v[26:27], v[142:143], v[16:17] op_sel_hi:[0,1]
	v_pk_mul_f32 v[16:17], v[142:143], v[14:15] op_sel_hi:[0,1]
	v_cvt_pk_bf16_f32 v14, v22, v23
	v_cvt_pk_bf16_f32 v15, v24, v25
	v_cvt_pk_bf16_f32 v16, v16, v17
	v_cvt_pk_bf16_f32 v17, v26, v27
	global_store_dwordx4 v[30:31], v[14:17], off offset:256 nt
	s_nop 1
	v_mad_i64_i32 v[14:15], s[22:23], v1, s48, v[144:145]
	v_lshl_add_u64 v[14:15], v[14:15], 0, v[146:147]
	v_pk_mul_f32 v[16:17], v[142:143], v[20:21] op_sel_hi:[0,1]
	v_pk_mul_f32 v[20:21], v[142:143], v[12:13] op_sel_hi:[0,1]
	v_pk_mul_f32 v[12:13], v[142:143], v[10:11] op_sel_hi:[0,1]
	v_cvt_pk_bf16_f32 v10, v18, v19
	v_cvt_pk_bf16_f32 v11, v16, v17
	v_cvt_pk_bf16_f32 v12, v12, v13
	v_cvt_pk_bf16_f32 v13, v20, v21
	global_store_dwordx4 v[14:15], v[10:13], off nt
	s_nop 1
	v_pk_mul_f32 v[10:11], v[142:143], v[4:5] op_sel_hi:[0,1]
	v_pk_mul_f32 v[4:5], v[142:143], v[2:3] op_sel_hi:[0,1]
	v_cvt_pk_bf16_f32 v2, v6, v7
	v_cvt_pk_bf16_f32 v3, v8, v9
	v_cvt_pk_bf16_f32 v4, v4, v5
	v_cvt_pk_bf16_f32 v5, v10, v11
	global_store_dwordx4 v[14:15], v[2:5], off offset:256 nt
	s_cbranch_vccnz .LBB0_385
	s_andn2_b64 vcc, exec, s[6:7]
	s_cbranch_vccnz .LBB0_370
	s_barrier
	s_branch .LBB0_370

.LBB0_419:
	v_lshl_add_u32 v14, s2, 8, v212
	v_mov_b64_e32 v[4:5], s[88:89]
	v_ashrrev_i32_e32 v195, 31, v194
	v_mad_i64_i32 v[4:5], s[0:1], v14, s54, v[4:5]
	v_lshl_add_u64 v[4:5], v[194:195], 1, v[4:5]
	v_cvt_pk_bf16_f32 v6, v6, v7
	v_cvt_pk_bf16_f32 v7, v10, v11
	v_cvt_pk_bf16_f32 v8, v8, v9
	v_cvt_pk_bf16_f32 v9, v12, v13
	global_store_dwordx4 v[4:5], v[6:9], off nt
	s_andn2_b64 vcc, exec, s[30:31]
	s_mov_b64 s[0:1], -1
	v_cndmask_b32_e64 v6, 0, 1, s[30:31]
	v_cmp_ne_u32_e64 s[4:5], 1, v6
	s_cbranch_vccnz .LBB0_421
	v_mov_b32_e32 v8, v2
	v_mov_b32_e32 v9, v2
	v_pk_mul_f32 v[10:11], v[8:9], v[172:173]
	v_pk_mul_f32 v[6:7], v[2:3], v[170:171]
	v_pk_mul_f32 v[12:13], v[8:9], v[168:169]
	v_pk_mul_f32 v[8:9], v[2:3], v[166:167]
	s_mov_b64 s[0:1], 0

.LBB0_423:
	v_cvt_pk_bf16_f32 v6, v6, v7
	v_cvt_pk_bf16_f32 v7, v10, v11
	v_cvt_pk_bf16_f32 v8, v8, v9
	v_cvt_pk_bf16_f32 v9, v12, v13
	s_and_b64 vcc, exec, s[4:5]
	s_mov_b64 s[0:1], -1
	global_store_dwordx4 v[4:5], v[6:9], off offset:256 nt
	s_cbranch_vccnz .LBB0_425
	v_mov_b32_e32 v4, v2
	v_mov_b32_e32 v5, v2
	v_pk_mul_f32 v[10:11], v[4:5], v[164:165]
	v_pk_mul_f32 v[6:7], v[2:3], v[162:163]
	v_pk_mul_f32 v[12:13], v[4:5], v[160:161]
	v_pk_mul_f32 v[8:9], v[2:3], v[158:159]
	s_mov_b64 s[0:1], 0

.LBB0_427:
	v_or_b32_e32 v15, 16, v14
	v_mov_b64_e32 v[4:5], s[88:89]
	v_mad_i64_i32 v[4:5], s[0:1], v15, s54, v[4:5]
	v_lshl_add_u64 v[4:5], v[194:195], 1, v[4:5]
	v_cvt_pk_bf16_f32 v6, v6, v7
	v_cvt_pk_bf16_f32 v7, v10, v11
	v_cvt_pk_bf16_f32 v8, v8, v9
	v_cvt_pk_bf16_f32 v9, v12, v13
	s_and_b64 vcc, exec, s[4:5]
	s_mov_b64 s[0:1], -1
	global_store_dwordx4 v[4:5], v[6:9], off nt
	s_cbranch_vccnz .LBB0_429
	s_nop 0
	v_mov_b32_e32 v8, v2
	v_mov_b32_e32 v9, v2
	v_pk_mul_f32 v[10:11], v[8:9], v[156:157]
	v_pk_mul_f32 v[6:7], v[2:3], v[154:155]
	v_pk_mul_f32 v[12:13], v[8:9], v[152:153]
	v_pk_mul_f32 v[8:9], v[2:3], v[150:151]
	s_mov_b64 s[0:1], 0

.LBB0_431:
	v_cvt_pk_bf16_f32 v6, v6, v7
	v_cvt_pk_bf16_f32 v7, v10, v11
	v_cvt_pk_bf16_f32 v8, v8, v9
	v_cvt_pk_bf16_f32 v9, v12, v13
	s_and_b64 vcc, exec, s[4:5]
	s_mov_b64 s[0:1], -1
	global_store_dwordx4 v[4:5], v[6:9], off offset:256 nt
	s_cbranch_vccnz .LBB0_433
	v_mov_b32_e32 v4, v2
	v_mov_b32_e32 v5, v2
	v_pk_mul_f32 v[10:11], v[4:5], v[148:149]
	v_pk_mul_f32 v[6:7], v[2:3], v[146:147]
	v_pk_mul_f32 v[12:13], v[4:5], v[144:145]
	v_pk_mul_f32 v[8:9], v[2:3], v[142:143]
	s_mov_b64 s[0:1], 0

.LBB0_435:
	v_or_b32_e32 v15, 32, v14
	v_mov_b64_e32 v[4:5], s[88:89]
	v_mad_i64_i32 v[4:5], s[0:1], v15, s54, v[4:5]
	v_lshl_add_u64 v[4:5], v[194:195], 1, v[4:5]
	v_cvt_pk_bf16_f32 v6, v6, v7
	v_cvt_pk_bf16_f32 v7, v10, v11
	v_cvt_pk_bf16_f32 v8, v8, v9
	v_cvt_pk_bf16_f32 v9, v12, v13
	s_and_b64 vcc, exec, s[4:5]
	s_mov_b64 s[0:1], -1
	global_store_dwordx4 v[4:5], v[6:9], off nt
	s_cbranch_vccnz .LBB0_437
	s_nop 0
	v_mov_b32_e32 v8, v2
	v_mov_b32_e32 v9, v2
	v_pk_mul_f32 v[10:11], v[8:9], v[140:141]
	v_pk_mul_f32 v[6:7], v[2:3], v[138:139]
	v_pk_mul_f32 v[12:13], v[8:9], v[136:137]
	v_pk_mul_f32 v[8:9], v[2:3], v[134:135]
	s_mov_b64 s[0:1], 0

.LBB0_439:
	v_cvt_pk_bf16_f32 v6, v6, v7
	v_cvt_pk_bf16_f32 v7, v10, v11
	v_cvt_pk_bf16_f32 v8, v8, v9
	v_cvt_pk_bf16_f32 v9, v12, v13
	s_and_b64 vcc, exec, s[4:5]
	s_mov_b64 s[0:1], -1
	global_store_dwordx4 v[4:5], v[6:9], off offset:256 nt
	s_cbranch_vccnz .LBB0_441
	v_mov_b32_e32 v4, v2
	v_mov_b32_e32 v5, v2
	v_pk_mul_f32 v[10:11], v[4:5], v[132:133]
	v_pk_mul_f32 v[6:7], v[2:3], v[130:131]
	v_pk_mul_f32 v[12:13], v[4:5], v[128:129]
	v_pk_mul_f32 v[8:9], v[2:3], v[126:127]
	s_mov_b64 s[0:1], 0

.LBB0_443:
	v_or_b32_e32 v15, 48, v14
	v_mov_b64_e32 v[4:5], s[88:89]
	v_mad_i64_i32 v[4:5], s[0:1], v15, s54, v[4:5]
	v_lshl_add_u64 v[4:5], v[194:195], 1, v[4:5]
	v_cvt_pk_bf16_f32 v6, v6, v7
	v_cvt_pk_bf16_f32 v7, v10, v11
	v_cvt_pk_bf16_f32 v8, v8, v9
	v_cvt_pk_bf16_f32 v9, v12, v13
	s_and_b64 vcc, exec, s[4:5]
	s_mov_b64 s[0:1], -1
	global_store_dwordx4 v[4:5], v[6:9], off nt
	s_cbranch_vccnz .LBB0_445
	s_nop 0
	v_mov_b32_e32 v8, v2
	v_mov_b32_e32 v9, v2
	v_pk_mul_f32 v[10:11], v[8:9], v[124:125]
	v_pk_mul_f32 v[6:7], v[2:3], v[122:123]
	v_pk_mul_f32 v[12:13], v[8:9], v[120:121]
	v_pk_mul_f32 v[8:9], v[2:3], v[118:119]
	s_mov_b64 s[0:1], 0

.LBB0_447:
	v_cvt_pk_bf16_f32 v6, v6, v7
	v_cvt_pk_bf16_f32 v7, v10, v11
	v_cvt_pk_bf16_f32 v8, v8, v9
	v_cvt_pk_bf16_f32 v9, v12, v13
	s_and_b64 vcc, exec, s[4:5]
	s_mov_b64 s[0:1], -1
	global_store_dwordx4 v[4:5], v[6:9], off offset:256 nt
	s_cbranch_vccnz .LBB0_449
	v_mov_b32_e32 v4, v2
	v_mov_b32_e32 v5, v2
	v_pk_mul_f32 v[10:11], v[4:5], v[116:117]
	v_pk_mul_f32 v[6:7], v[2:3], v[114:115]
	v_pk_mul_f32 v[12:13], v[4:5], v[112:113]
	v_pk_mul_f32 v[8:9], v[2:3], v[110:111]
	s_mov_b64 s[0:1], 0

.LBB0_451:
	v_add_u32_e32 v15, 0x80, v14
	v_mov_b64_e32 v[4:5], s[88:89]
	v_mad_i64_i32 v[4:5], s[0:1], v15, s54, v[4:5]
	v_lshl_add_u64 v[4:5], v[194:195], 1, v[4:5]
	v_cvt_pk_bf16_f32 v6, v6, v7
	v_cvt_pk_bf16_f32 v7, v10, v11
	v_cvt_pk_bf16_f32 v8, v8, v9
	v_cvt_pk_bf16_f32 v9, v12, v13
	s_and_b64 vcc, exec, s[4:5]
	s_mov_b64 s[0:1], -1
	global_store_dwordx4 v[4:5], v[6:9], off nt
	s_cbranch_vccnz .LBB0_453
	s_nop 0
	v_mov_b32_e32 v8, v2
	v_mov_b32_e32 v9, v2
	v_pk_mul_f32 v[10:11], v[8:9], v[108:109]
	v_pk_mul_f32 v[6:7], v[2:3], v[106:107]
	v_pk_mul_f32 v[12:13], v[8:9], v[104:105]
	v_pk_mul_f32 v[8:9], v[2:3], v[102:103]
	s_mov_b64 s[0:1], 0

.LBB0_455:
	v_cvt_pk_bf16_f32 v6, v6, v7
	v_cvt_pk_bf16_f32 v7, v10, v11
	v_cvt_pk_bf16_f32 v8, v8, v9
	v_cvt_pk_bf16_f32 v9, v12, v13
	s_and_b64 vcc, exec, s[4:5]
	s_mov_b64 s[0:1], -1
	global_store_dwordx4 v[4:5], v[6:9], off offset:256 nt
	s_cbranch_vccnz .LBB0_457
	v_mov_b32_e32 v4, v2
	v_mov_b32_e32 v5, v2
	v_pk_mul_f32 v[10:11], v[4:5], v[100:101]
	v_pk_mul_f32 v[6:7], v[2:3], v[98:99]
	v_pk_mul_f32 v[12:13], v[4:5], v[96:97]
	v_pk_mul_f32 v[8:9], v[2:3], v[94:95]
	s_mov_b64 s[0:1], 0

.LBB0_459:
	v_add_u32_e32 v15, 0x90, v14
	v_mov_b64_e32 v[4:5], s[88:89]
	v_mad_i64_i32 v[4:5], s[0:1], v15, s54, v[4:5]
	v_lshl_add_u64 v[4:5], v[194:195], 1, v[4:5]
	v_cvt_pk_bf16_f32 v6, v6, v7
	v_cvt_pk_bf16_f32 v7, v10, v11
	v_cvt_pk_bf16_f32 v8, v8, v9
	v_cvt_pk_bf16_f32 v9, v12, v13
	s_and_b64 vcc, exec, s[4:5]
	s_mov_b64 s[0:1], -1
	global_store_dwordx4 v[4:5], v[6:9], off nt
	s_cbranch_vccnz .LBB0_461
	s_nop 0
	v_mov_b32_e32 v8, v2
	v_mov_b32_e32 v9, v2
	v_pk_mul_f32 v[10:11], v[8:9], v[92:93]
	v_pk_mul_f32 v[6:7], v[2:3], v[90:91]
	v_pk_mul_f32 v[12:13], v[8:9], v[88:89]
	v_pk_mul_f32 v[8:9], v[2:3], v[86:87]
	s_mov_b64 s[0:1], 0

.LBB0_463:
	v_cvt_pk_bf16_f32 v6, v6, v7
	v_cvt_pk_bf16_f32 v7, v10, v11
	v_cvt_pk_bf16_f32 v8, v8, v9
	v_cvt_pk_bf16_f32 v9, v12, v13
	s_and_b64 vcc, exec, s[4:5]
	s_mov_b64 s[0:1], -1
	global_store_dwordx4 v[4:5], v[6:9], off offset:256 nt
	s_cbranch_vccnz .LBB0_465
	v_mov_b32_e32 v4, v2
	v_mov_b32_e32 v5, v2
	v_pk_mul_f32 v[10:11], v[4:5], v[84:85]
	v_pk_mul_f32 v[6:7], v[2:3], v[82:83]
	v_pk_mul_f32 v[12:13], v[4:5], v[80:81]
	v_pk_mul_f32 v[8:9], v[2:3], v[78:79]
	s_mov_b64 s[0:1], 0

.LBB0_467:
	v_add_u32_e32 v15, 0xa0, v14
	v_mov_b64_e32 v[4:5], s[88:89]
	v_mad_i64_i32 v[4:5], s[0:1], v15, s54, v[4:5]
	v_lshl_add_u64 v[4:5], v[194:195], 1, v[4:5]
	v_cvt_pk_bf16_f32 v6, v6, v7
	v_cvt_pk_bf16_f32 v7, v10, v11
	v_cvt_pk_bf16_f32 v8, v8, v9
	v_cvt_pk_bf16_f32 v9, v12, v13
	s_and_b64 vcc, exec, s[4:5]
	s_mov_b64 s[0:1], -1
	global_store_dwordx4 v[4:5], v[6:9], off nt
	s_cbranch_vccnz .LBB0_469
	s_nop 0
	v_mov_b32_e32 v8, v2
	v_mov_b32_e32 v9, v2
	v_pk_mul_f32 v[10:11], v[8:9], v[76:77]
	v_pk_mul_f32 v[6:7], v[2:3], v[74:75]
	v_pk_mul_f32 v[12:13], v[8:9], v[72:73]
	v_pk_mul_f32 v[8:9], v[2:3], v[70:71]
	s_mov_b64 s[0:1], 0

.LBB0_471:
	v_cvt_pk_bf16_f32 v6, v6, v7
	v_cvt_pk_bf16_f32 v7, v10, v11
	v_cvt_pk_bf16_f32 v8, v8, v9
	v_cvt_pk_bf16_f32 v9, v12, v13
	s_and_b64 vcc, exec, s[4:5]
	s_mov_b64 s[0:1], -1
	global_store_dwordx4 v[4:5], v[6:9], off offset:256 nt
	s_cbranch_vccnz .LBB0_473
	v_mov_b32_e32 v4, v2
	v_mov_b32_e32 v5, v2
	v_pk_mul_f32 v[10:11], v[4:5], v[68:69]
	v_pk_mul_f32 v[6:7], v[2:3], v[66:67]
	v_pk_mul_f32 v[12:13], v[4:5], v[64:65]
	v_pk_mul_f32 v[8:9], v[2:3], v[62:63]
	s_mov_b64 s[0:1], 0

.LBB0_475:
	v_add_u32_e32 v14, 0xb0, v14
	v_mov_b64_e32 v[4:5], s[88:89]
	v_mad_i64_i32 v[4:5], s[0:1], v14, s54, v[4:5]
	v_lshl_add_u64 v[4:5], v[194:195], 1, v[4:5]
	v_cvt_pk_bf16_f32 v6, v6, v7
	v_cvt_pk_bf16_f32 v7, v10, v11
	v_cvt_pk_bf16_f32 v8, v8, v9
	v_cvt_pk_bf16_f32 v9, v12, v13
	s_and_b64 vcc, exec, s[4:5]
	s_mov_b64 s[0:1], -1
	global_store_dwordx4 v[4:5], v[6:9], off nt
	s_cbranch_vccnz .LBB0_477
	s_nop 0
	v_mov_b32_e32 v8, v2
	v_mov_b32_e32 v9, v2
	v_pk_mul_f32 v[10:11], v[8:9], v[60:61]
	v_pk_mul_f32 v[6:7], v[2:3], v[58:59]
	v_pk_mul_f32 v[12:13], v[8:9], v[56:57]
	v_pk_mul_f32 v[8:9], v[2:3], v[54:55]
	s_mov_b64 s[0:1], 0

.LBB0_479:
	s_and_b64 vcc, exec, s[6:7]
	v_cvt_pk_bf16_f32 v6, v6, v7
	v_cvt_pk_bf16_f32 v7, v10, v11
	v_cvt_pk_bf16_f32 v8, v8, v9
	v_cvt_pk_bf16_f32 v9, v12, v13
	global_store_dwordx4 v[4:5], v[6:9], off offset:256 nt
	s_cbranch_vccnz .LBB0_482
	s_andn2_b64 vcc, exec, s[18:19]
	s_cbranch_vccnz .LBB0_393
	s_barrier
	s_branch .LBB0_393

.LBB0_923:
	v_mul_lo_u32 v143, v221, s41
	v_lshl_add_u32 v143, v206, 1, v143
	v_add_u32_e32 v143, 0x2000, v143
	s_mov_b64 s[98:99], s[12:13]
	global_load_dwordx4 v[144:147], v143, s[98:99]
	global_load_dwordx4 v[148:151], v143, s[98:99] offset:256
	s_add_u32 s98, s98, 0x68800
	s_addc_u32 s99, s99, 0
	global_load_dwordx4 v[152:155], v143, s[98:99]
	global_load_dwordx4 v[156:159], v143, s[98:99] offset:256
	s_add_u32 s98, s98, 0x68800
	s_addc_u32 s99, s99, 0
	global_load_dwordx4 v[160:163], v143, s[98:99]
	global_load_dwordx4 v[164:167], v143, s[98:99] offset:256
	s_add_u32 s98, s98, 0x68800
	s_addc_u32 s99, s99, 0
	global_load_dwordx4 v[168:171], v143, s[98:99]
	global_load_dwordx4 v[172:175], v143, s[98:99] offset:256
	s_add_u32 s98, s98, 0x20a800
	s_addc_u32 s99, s99, 0
	global_load_dwordx4 v[176:179], v143, s[98:99]
	global_load_dwordx4 v[180:183], v143, s[98:99] offset:256
	s_add_u32 s98, s98, 0x68800
	s_addc_u32 s99, s99, 0
	global_load_dwordx4 v[184:187], v143, s[98:99]
	global_load_dwordx4 v[188:191], v143, s[98:99] offset:256
	s_add_u32 s98, s98, 0x68800
	s_addc_u32 s99, s99, 0
	global_load_dwordx4 v[222:225], v143, s[98:99]
	global_load_dwordx4 v[226:229], v143, s[98:99] offset:256
	s_add_u32 s98, s98, 0x68800
	s_addc_u32 s99, s99, 0
	global_load_dwordx4 v[230:233], v143, s[98:99]
	global_load_dwordx4 v[234:237], v143, s[98:99] offset:256
	v_mov_b64_e32 v[132:133], s[12:13]
	v_mad_i64_i32 v[134:135], s[22:23], v221, s41, v[132:133]
	v_lshlrev_b64 v[130:131], 1, v[206:207]
	v_lshl_add_u64 v[134:135], v[134:135], 0, v[130:131]
	v_add_co_u32_e32 v138, vcc, 0x2000, v134
	s_nop 1
	v_addc_co_u32_e32 v139, vcc, 0, v135, vcc
	s_waitcnt vmcnt(15)
	v_lshlrev_b32_e32 v1, 16, v144
	v_and_b32_e32 v134, 0xffff0000, v144
	v_lshlrev_b32_e32 v140, 16, v145
	v_lshlrev_b32_e32 v142, 16, v147
	v_and_b32_e32 v137, 0xffff0000, v147
	v_and_b32_e32 v135, 0xffff0000, v145
	v_lshlrev_b32_e32 v141, 16, v146
	v_and_b32_e32 v136, 0xffff0000, v146
	v_mul_f32_e32 v1, v126, v1
	v_mul_f32_e32 v126, v127, v134
	v_mul_f32_e32 v127, v128, v140
	v_mul_f32_e32 v134, v125, v137
	v_mul_f32_e32 v128, v129, v135
	v_mul_f32_e32 v122, v122, v141
	v_mul_f32_e32 v123, v123, v136
	v_mul_f32_e32 v129, v124, v142
	v_cvt_pk_bf16_f32 v124, v1, v126
	v_cvt_pk_bf16_f32 v125, v127, v128
	v_cvt_pk_bf16_f32 v126, v122, v123
	v_cvt_pk_bf16_f32 v127, v129, v134
	v_mov_b64_e32 v[122:123], s[4:5]
	v_or_b32_e32 v1, 16, v221
	v_mad_i64_i32 v[128:129], s[22:23], v221, s46, v[122:123]
	v_mad_i64_i32 v[138:139], s[22:23], v1, s41, v[132:133]
	v_lshl_add_u64 v[128:129], v[128:129], 0, v[130:131]
	v_lshl_add_u64 v[138:139], v[138:139], 0, v[130:131]
	v_add_co_u32_e32 v138, vcc, s39, v138
	global_store_dwordx4 v[128:129], v[124:127], off nt
	s_nop 0
	v_addc_co_u32_e32 v139, vcc, 0, v139, vcc
	s_waitcnt vmcnt(15)
	v_lshlrev_b32_e32 v124, 16, v148
	v_and_b32_e32 v125, 0xffff0000, v148
	v_lshlrev_b32_e32 v126, 16, v149
	v_and_b32_e32 v127, 0xffff0000, v149
	v_lshlrev_b32_e32 v134, 16, v150
	v_and_b32_e32 v135, 0xffff0000, v150
	v_lshlrev_b32_e32 v136, 16, v151
	v_and_b32_e32 v137, 0xffff0000, v151
	v_mul_f32_e32 v118, v118, v124
	v_mul_f32_e32 v119, v119, v125
	v_mul_f32_e32 v120, v120, v126
	v_mul_f32_e32 v121, v121, v127
	v_mul_f32_e32 v113, v113, v137
	v_mul_f32_e32 v124, v110, v134
	v_mul_f32_e32 v125, v111, v135
	v_mul_f32_e32 v126, v112, v136
	v_cvt_pk_bf16_f32 v110, v118, v119
	v_cvt_pk_bf16_f32 v111, v120, v121
	v_cvt_pk_bf16_f32 v112, v124, v125
	v_cvt_pk_bf16_f32 v113, v126, v113
	s_nop 0
	global_store_dwordx4 v[128:129], v[110:113], off offset:256 nt
	s_waitcnt vmcnt(15)
	s_nop 0
	v_lshlrev_b32_e32 v110, 16, v152
	v_and_b32_e32 v111, 0xffff0000, v152
	v_lshlrev_b32_e32 v112, 16, v153
	v_and_b32_e32 v113, 0xffff0000, v153
	v_lshlrev_b32_e32 v118, 16, v154
	v_and_b32_e32 v119, 0xffff0000, v154
	v_lshlrev_b32_e32 v120, 16, v155
	v_and_b32_e32 v121, 0xffff0000, v155
	v_mul_f32_e32 v110, v114, v110
	v_mul_f32_e32 v111, v115, v111
	v_mul_f32_e32 v112, v116, v112
	v_mul_f32_e32 v113, v117, v113
	v_mul_f32_e32 v109, v109, v121
	v_mul_f32_e32 v114, v106, v118
	v_mul_f32_e32 v115, v107, v119
	v_mul_f32_e32 v116, v108, v120
	v_cvt_pk_bf16_f32 v106, v110, v111
	v_cvt_pk_bf16_f32 v107, v112, v113
	v_cvt_pk_bf16_f32 v108, v114, v115
	v_cvt_pk_bf16_f32 v109, v116, v109
	v_or_b32_e32 v118, 32, v221
	v_mad_i64_i32 v[114:115], s[22:23], v1, s46, v[122:123]
	v_mad_i64_i32 v[116:117], s[22:23], v118, s41, v[132:133]
	v_lshl_add_u64 v[114:115], v[114:115], 0, v[130:131]
	v_lshl_add_u64 v[116:117], v[116:117], 0, v[130:131]
	v_add_co_u32_e32 v116, vcc, s39, v116
	global_store_dwordx4 v[114:115], v[106:109], off nt
	s_nop 0
	v_addc_co_u32_e32 v117, vcc, 0, v117, vcc
	s_waitcnt vmcnt(15)
	v_lshlrev_b32_e32 v1, 16, v156
	v_and_b32_e32 v106, 0xffff0000, v156
	v_lshlrev_b32_e32 v107, 16, v157
	v_and_b32_e32 v108, 0xffff0000, v157
	v_lshlrev_b32_e32 v109, 16, v158
	v_and_b32_e32 v110, 0xffff0000, v158
	v_and_b32_e32 v112, 0xffff0000, v159
	v_lshlrev_b32_e32 v111, 16, v159
	v_mul_f32_e32 v1, v102, v1
	v_mul_f32_e32 v102, v103, v106
	v_mul_f32_e32 v103, v104, v107
	v_mul_f32_e32 v104, v105, v108
	v_mul_f32_e32 v105, v94, v109
	v_mul_f32_e32 v97, v97, v112
	v_mul_f32_e32 v106, v95, v110
	v_mul_f32_e32 v107, v96, v111
	v_cvt_pk_bf16_f32 v94, v1, v102
	v_cvt_pk_bf16_f32 v95, v103, v104
	v_cvt_pk_bf16_f32 v96, v105, v106
	v_cvt_pk_bf16_f32 v97, v107, v97
	s_waitcnt vmcnt(15)
	v_lshlrev_b32_e32 v1, 16, v160
	global_store_dwordx4 v[114:115], v[94:97], off offset:256 nt
	v_mul_f32_e32 v1, v98, v1
	s_nop 0
	v_and_b32_e32 v94, 0xffff0000, v160
	v_lshlrev_b32_e32 v95, 16, v161
	v_and_b32_e32 v96, 0xffff0000, v161
	v_lshlrev_b32_e32 v97, 16, v162
	v_and_b32_e32 v102, 0xffff0000, v162
	v_and_b32_e32 v104, 0xffff0000, v163
	v_lshlrev_b32_e32 v103, 16, v163
	v_mul_f32_e32 v94, v99, v94
	v_mul_f32_e32 v95, v100, v95
	v_mul_f32_e32 v96, v101, v96
	v_mul_f32_e32 v97, v90, v97
	v_mul_f32_e32 v93, v93, v104
	v_mul_f32_e32 v98, v91, v102
	v_mul_f32_e32 v99, v92, v103
	v_cvt_pk_bf16_f32 v90, v1, v94
	v_cvt_pk_bf16_f32 v91, v95, v96
	v_cvt_pk_bf16_f32 v92, v97, v98
	v_cvt_pk_bf16_f32 v93, v99, v93
	v_or_b32_e32 v1, 48, v221
	v_mad_i64_i32 v[98:99], s[22:23], v118, s46, v[122:123]
	v_mad_i64_i32 v[100:101], s[22:23], v1, s41, v[132:133]
	v_lshl_add_u64 v[98:99], v[98:99], 0, v[130:131]
	v_lshl_add_u64 v[100:101], v[100:101], 0, v[130:131]
	v_add_co_u32_e32 v100, vcc, s39, v100
	global_store_dwordx4 v[98:99], v[90:93], off nt
	s_nop 0
	v_addc_co_u32_e32 v101, vcc, 0, v101, vcc
	s_waitcnt vmcnt(15)
	v_lshlrev_b32_e32 v90, 16, v164
	v_and_b32_e32 v91, 0xffff0000, v164
	v_lshlrev_b32_e32 v92, 16, v165
	v_and_b32_e32 v93, 0xffff0000, v165
	v_lshlrev_b32_e32 v94, 16, v166
	v_and_b32_e32 v95, 0xffff0000, v166
	v_lshlrev_b32_e32 v96, 16, v167
	v_and_b32_e32 v97, 0xffff0000, v167
	v_mul_f32_e32 v86, v86, v90
	v_mul_f32_e32 v87, v87, v91
	v_mul_f32_e32 v88, v88, v92
	v_mul_f32_e32 v89, v89, v93
	v_mul_f32_e32 v81, v81, v97
	v_mul_f32_e32 v90, v78, v94
	v_mul_f32_e32 v91, v79, v95
	v_mul_f32_e32 v92, v80, v96
	v_cvt_pk_bf16_f32 v78, v86, v87
	v_cvt_pk_bf16_f32 v79, v88, v89
	v_cvt_pk_bf16_f32 v80, v90, v91
	v_cvt_pk_bf16_f32 v81, v92, v81
	s_nop 0
	global_store_dwordx4 v[98:99], v[78:81], off offset:256 nt
	s_waitcnt vmcnt(15)
	s_nop 0
	v_lshlrev_b32_e32 v78, 16, v168
	v_and_b32_e32 v79, 0xffff0000, v168
	v_lshlrev_b32_e32 v80, 16, v169
	v_and_b32_e32 v81, 0xffff0000, v169
	v_lshlrev_b32_e32 v86, 16, v170
	v_and_b32_e32 v87, 0xffff0000, v170
	v_lshlrev_b32_e32 v88, 16, v171
	v_and_b32_e32 v89, 0xffff0000, v171
	v_mul_f32_e32 v78, v82, v78
	v_mul_f32_e32 v79, v83, v79
	v_mul_f32_e32 v80, v84, v80
	v_mul_f32_e32 v81, v85, v81
	v_mul_f32_e32 v77, v77, v89
	v_mul_f32_e32 v82, v74, v86
	v_mul_f32_e32 v83, v75, v87
	v_mul_f32_e32 v84, v76, v88
	v_cvt_pk_bf16_f32 v74, v78, v79
	v_cvt_pk_bf16_f32 v75, v80, v81
	v_cvt_pk_bf16_f32 v76, v82, v83
	v_cvt_pk_bf16_f32 v77, v84, v77
	v_add_u32_e32 v86, 0x80, v221
	v_mad_i64_i32 v[82:83], s[22:23], v1, s46, v[122:123]
	v_mad_i64_i32 v[84:85], s[22:23], v86, s41, v[132:133]
	v_lshl_add_u64 v[82:83], v[82:83], 0, v[130:131]
	v_lshl_add_u64 v[84:85], v[84:85], 0, v[130:131]
	v_add_co_u32_e32 v84, vcc, s39, v84
	global_store_dwordx4 v[82:83], v[74:77], off nt
	s_nop 0
	v_addc_co_u32_e32 v85, vcc, 0, v85, vcc
	s_waitcnt vmcnt(15)
	v_lshlrev_b32_e32 v1, 16, v172
	v_and_b32_e32 v74, 0xffff0000, v172
	v_lshlrev_b32_e32 v75, 16, v173
	v_and_b32_e32 v76, 0xffff0000, v173
	v_lshlrev_b32_e32 v77, 16, v174
	v_and_b32_e32 v78, 0xffff0000, v174
	v_and_b32_e32 v80, 0xffff0000, v175
	v_lshlrev_b32_e32 v79, 16, v175
	v_mul_f32_e32 v1, v70, v1
	v_mul_f32_e32 v70, v71, v74
	v_mul_f32_e32 v71, v72, v75
	v_mul_f32_e32 v72, v73, v76
	v_mul_f32_e32 v73, v66, v77
	v_mul_f32_e32 v69, v69, v80
	v_mul_f32_e32 v74, v67, v78
	v_mul_f32_e32 v75, v68, v79
	v_cvt_pk_bf16_f32 v66, v1, v70
	v_cvt_pk_bf16_f32 v67, v71, v72
	v_cvt_pk_bf16_f32 v68, v73, v74
	v_cvt_pk_bf16_f32 v69, v75, v69
	s_waitcnt vmcnt(15)
	v_lshlrev_b32_e32 v1, 16, v176
	global_store_dwordx4 v[82:83], v[66:69], off offset:256 nt
	v_mul_f32_e32 v1, v62, v1
	s_nop 0
	v_and_b32_e32 v66, 0xffff0000, v176
	v_lshlrev_b32_e32 v67, 16, v177
	v_and_b32_e32 v68, 0xffff0000, v177
	v_lshlrev_b32_e32 v69, 16, v178
	v_and_b32_e32 v70, 0xffff0000, v178
	v_and_b32_e32 v72, 0xffff0000, v179
	v_lshlrev_b32_e32 v71, 16, v179
	v_mul_f32_e32 v62, v63, v66
	v_mul_f32_e32 v63, v64, v67
	v_mul_f32_e32 v64, v65, v68
	v_mul_f32_e32 v65, v58, v69
	v_mul_f32_e32 v61, v61, v72
	v_mul_f32_e32 v66, v59, v70
	v_mul_f32_e32 v67, v60, v71
	v_cvt_pk_bf16_f32 v58, v1, v62
	v_cvt_pk_bf16_f32 v59, v63, v64
	v_cvt_pk_bf16_f32 v60, v65, v66
	v_cvt_pk_bf16_f32 v61, v67, v61
	v_add_u32_e32 v1, 0x90, v221
	v_mad_i64_i32 v[66:67], s[22:23], v86, s46, v[122:123]
	v_mad_i64_i32 v[68:69], s[22:23], v1, s41, v[132:133]
	v_lshl_add_u64 v[66:67], v[66:67], 0, v[130:131]
	v_lshl_add_u64 v[68:69], v[68:69], 0, v[130:131]
	v_add_co_u32_e32 v68, vcc, s39, v68
	global_store_dwordx4 v[66:67], v[58:61], off nt
	s_nop 0
	v_addc_co_u32_e32 v69, vcc, 0, v69, vcc
	s_waitcnt vmcnt(15)
	v_lshlrev_b32_e32 v58, 16, v180
	v_and_b32_e32 v59, 0xffff0000, v180
	v_lshlrev_b32_e32 v60, 16, v181
	v_and_b32_e32 v61, 0xffff0000, v181
	v_lshlrev_b32_e32 v62, 16, v182
	v_and_b32_e32 v63, 0xffff0000, v182
	v_lshlrev_b32_e32 v64, 16, v183
	v_and_b32_e32 v65, 0xffff0000, v183
	v_mul_f32_e32 v54, v54, v58
	v_mul_f32_e32 v55, v55, v59
	v_mul_f32_e32 v56, v56, v60
	v_mul_f32_e32 v57, v57, v61
	v_mul_f32_e32 v49, v49, v65
	v_mul_f32_e32 v58, v46, v62
	v_mul_f32_e32 v59, v47, v63
	v_mul_f32_e32 v60, v48, v64
	v_cvt_pk_bf16_f32 v46, v54, v55
	v_cvt_pk_bf16_f32 v47, v56, v57
	v_cvt_pk_bf16_f32 v48, v58, v59
	v_cvt_pk_bf16_f32 v49, v60, v49
	s_nop 0
	global_store_dwordx4 v[66:67], v[46:49], off offset:256 nt
	s_waitcnt vmcnt(15)
	s_nop 0
	v_lshlrev_b32_e32 v46, 16, v184
	v_and_b32_e32 v47, 0xffff0000, v184
	v_lshlrev_b32_e32 v48, 16, v185
	v_and_b32_e32 v49, 0xffff0000, v185
	v_lshlrev_b32_e32 v54, 16, v186
	v_and_b32_e32 v55, 0xffff0000, v186
	v_lshlrev_b32_e32 v56, 16, v187
	v_and_b32_e32 v57, 0xffff0000, v187
	v_mul_f32_e32 v46, v50, v46
	v_mul_f32_e32 v47, v51, v47
	v_mul_f32_e32 v48, v52, v48
	v_mul_f32_e32 v49, v53, v49
	v_mul_f32_e32 v45, v45, v57
	v_mul_f32_e32 v50, v42, v54
	v_mul_f32_e32 v51, v43, v55
	v_mul_f32_e32 v52, v44, v56
	v_cvt_pk_bf16_f32 v42, v46, v47
	v_cvt_pk_bf16_f32 v43, v48, v49
	v_cvt_pk_bf16_f32 v44, v50, v51
	v_cvt_pk_bf16_f32 v45, v52, v45
	v_add_u32_e32 v54, 0xa0, v221
	v_mad_i64_i32 v[50:51], s[22:23], v1, s46, v[122:123]
	v_mad_i64_i32 v[52:53], s[22:23], v54, s41, v[132:133]
	v_lshl_add_u64 v[50:51], v[50:51], 0, v[130:131]
	v_lshl_add_u64 v[52:53], v[52:53], 0, v[130:131]
	v_add_co_u32_e32 v52, vcc, s39, v52
	global_store_dwordx4 v[50:51], v[42:45], off nt
	s_nop 0
	v_addc_co_u32_e32 v53, vcc, 0, v53, vcc
	s_waitcnt vmcnt(15)
	v_lshlrev_b32_e32 v1, 16, v188
	v_and_b32_e32 v42, 0xffff0000, v188
	v_lshlrev_b32_e32 v43, 16, v189
	v_and_b32_e32 v44, 0xffff0000, v189
	v_lshlrev_b32_e32 v45, 16, v190
	v_and_b32_e32 v46, 0xffff0000, v190
	v_and_b32_e32 v48, 0xffff0000, v191
	v_lshlrev_b32_e32 v47, 16, v191
	v_mul_f32_e32 v1, v38, v1
	v_mul_f32_e32 v38, v39, v42
	v_mul_f32_e32 v39, v40, v43
	v_mul_f32_e32 v40, v41, v44
	v_mul_f32_e32 v41, v30, v45
	v_mul_f32_e32 v33, v33, v48
	v_mul_f32_e32 v42, v31, v46
	v_mul_f32_e32 v43, v32, v47
	v_cvt_pk_bf16_f32 v30, v1, v38
	v_cvt_pk_bf16_f32 v31, v39, v40
	v_cvt_pk_bf16_f32 v32, v41, v42
	v_cvt_pk_bf16_f32 v33, v43, v33
	s_waitcnt vmcnt(15)
	v_lshlrev_b32_e32 v1, 16, v222
	global_store_dwordx4 v[50:51], v[30:33], off offset:256 nt
	v_mul_f32_e32 v1, v34, v1
	s_nop 0
	v_and_b32_e32 v30, 0xffff0000, v222
	v_lshlrev_b32_e32 v31, 16, v223
	v_and_b32_e32 v32, 0xffff0000, v223
	v_lshlrev_b32_e32 v33, 16, v224
	v_and_b32_e32 v38, 0xffff0000, v224
	v_and_b32_e32 v40, 0xffff0000, v225
	v_lshlrev_b32_e32 v39, 16, v225
	v_mul_f32_e32 v30, v35, v30
	v_mul_f32_e32 v31, v36, v31
	v_mul_f32_e32 v32, v37, v32
	v_mul_f32_e32 v33, v26, v33
	v_mul_f32_e32 v29, v29, v40
	v_mul_f32_e32 v34, v27, v38
	v_mul_f32_e32 v35, v28, v39
	v_cvt_pk_bf16_f32 v26, v1, v30
	v_cvt_pk_bf16_f32 v27, v31, v32
	v_cvt_pk_bf16_f32 v28, v33, v34
	v_cvt_pk_bf16_f32 v29, v35, v29
	v_add_u32_e32 v1, 0xb0, v221
	v_mad_i64_i32 v[34:35], s[22:23], v54, s46, v[122:123]
	v_mad_i64_i32 v[36:37], s[22:23], v1, s41, v[132:133]
	v_lshl_add_u64 v[34:35], v[34:35], 0, v[130:131]
	v_lshl_add_u64 v[36:37], v[36:37], 0, v[130:131]
	v_add_co_u32_e32 v36, vcc, s39, v36
	global_store_dwordx4 v[34:35], v[26:29], off nt
	s_nop 0
	v_addc_co_u32_e32 v37, vcc, 0, v37, vcc
	s_and_b64 vcc, exec, s[0:1]
	s_waitcnt vmcnt(15)
	v_lshlrev_b32_e32 v26, 16, v226
	v_and_b32_e32 v27, 0xffff0000, v226
	v_lshlrev_b32_e32 v28, 16, v227
	v_and_b32_e32 v29, 0xffff0000, v227
	v_lshlrev_b32_e32 v30, 16, v228
	v_and_b32_e32 v31, 0xffff0000, v228
	v_lshlrev_b32_e32 v32, 16, v229
	v_and_b32_e32 v33, 0xffff0000, v229
	v_mul_f32_e32 v22, v22, v26
	v_mul_f32_e32 v23, v23, v27
	v_mul_f32_e32 v24, v24, v28
	v_mul_f32_e32 v25, v25, v29
	v_mul_f32_e32 v17, v17, v33
	v_mul_f32_e32 v26, v14, v30
	v_mul_f32_e32 v27, v15, v31
	v_mul_f32_e32 v28, v16, v32
	v_cvt_pk_bf16_f32 v14, v22, v23
	v_cvt_pk_bf16_f32 v15, v24, v25
	v_cvt_pk_bf16_f32 v16, v26, v27
	v_cvt_pk_bf16_f32 v17, v28, v17
	s_nop 0
	global_store_dwordx4 v[34:35], v[14:17], off offset:256 nt
	s_waitcnt vmcnt(15)
	s_nop 0
	v_lshlrev_b32_e32 v14, 16, v230
	v_and_b32_e32 v15, 0xffff0000, v230
	v_lshlrev_b32_e32 v16, 16, v231
	v_and_b32_e32 v17, 0xffff0000, v231
	v_lshlrev_b32_e32 v22, 16, v232
	v_and_b32_e32 v23, 0xffff0000, v232
	v_lshlrev_b32_e32 v24, 16, v233
	v_and_b32_e32 v25, 0xffff0000, v233
	v_mul_f32_e32 v14, v18, v14
	v_mul_f32_e32 v15, v19, v15
	v_mul_f32_e32 v16, v20, v16
	v_mul_f32_e32 v17, v21, v17
	v_mul_f32_e32 v13, v13, v25
	v_mul_f32_e32 v18, v10, v22
	v_mul_f32_e32 v19, v11, v23
	v_mul_f32_e32 v20, v12, v24
	v_cvt_pk_bf16_f32 v10, v14, v15
	v_cvt_pk_bf16_f32 v11, v16, v17
	v_cvt_pk_bf16_f32 v12, v18, v19
	v_cvt_pk_bf16_f32 v13, v20, v13
	v_mad_i64_i32 v[18:19], s[22:23], v1, s46, v[122:123]
	v_lshl_add_u64 v[18:19], v[18:19], 0, v[130:131]
	global_store_dwordx4 v[18:19], v[10:13], off nt
	s_waitcnt vmcnt(15)
	v_lshlrev_b32_e32 v1, 16, v234
	v_and_b32_e32 v10, 0xffff0000, v234
	v_lshlrev_b32_e32 v13, 16, v236
	v_and_b32_e32 v14, 0xffff0000, v236
	v_and_b32_e32 v16, 0xffff0000, v237
	v_lshlrev_b32_e32 v11, 16, v235
	v_and_b32_e32 v12, 0xffff0000, v235
	v_lshlrev_b32_e32 v15, 16, v237
	v_mul_f32_e32 v5, v5, v16
	v_mul_f32_e32 v1, v6, v1
	v_mul_f32_e32 v6, v7, v10
	v_mul_f32_e32 v7, v8, v11
	v_mul_f32_e32 v8, v9, v12
	v_mul_f32_e32 v9, v2, v13
	v_mul_f32_e32 v10, v3, v14
	v_mul_f32_e32 v11, v4, v15
	v_cvt_pk_bf16_f32 v2, v1, v6
	v_cvt_pk_bf16_f32 v3, v7, v8
	v_cvt_pk_bf16_f32 v4, v9, v10
	v_cvt_pk_bf16_f32 v5, v11, v5
	global_store_dwordx4 v[18:19], v[2:5], off offset:256 nt
	s_cbranch_vccnz .LBB0_926
	s_andn2_b64 vcc, exec, s[10:11]
	s_cbranch_vccnz .LBB0_903
	s_barrier
	s_branch .LBB0_903

.LBB0_1001:
	v_lshl_add_u32 v140, s44, 8, v142
	v_lshl_or_b32 v138, s45, 8, v143
	v_lshl_add_u32 v150, v140, 11, v138
	v_lshlrev_b32_e32 v150, 2, v150
	v_readlane_b32 s44, v254, 12
	v_readlane_b32 s45, v254, 13
	v_readlane_b32 s46, v254, 14
	v_readlane_b32 s47, v254, 15
	v_readlane_b32 s48, v254, 16
	v_readlane_b32 s49, v254, 17
	v_readlane_b32 s50, v254, 18
	v_readlane_b32 s51, v254, 19
	v_readlane_b32 s52, v254, 20
	v_readlane_b32 s53, v254, 21
	v_readlane_b32 s54, v254, 22
	v_readlane_b32 s55, v254, 23
	v_readlane_b32 s56, v254, 24
	v_readlane_b32 s57, v254, 25
	v_readlane_b32 s58, v254, 26
	v_readlane_b32 s59, v254, 27
	s_and_b64 vcc, exec, s[2:3]
	s_mov_b64 s[98:99], s[44:45]
	s_mov_b64 s[100:101], s[0:1]
	global_load_dwordx4 v[154:157], v150, s[98:99]
	global_load_dwordx4 v[158:161], v150, s[98:99] offset:64
	global_load_dwordx4 v[162:165], v150, s[98:99] offset:512
	global_load_dwordx4 v[166:169], v150, s[98:99] offset:576
	s_add_u32 s98, s98, 0x20000
	s_addc_u32 s99, s99, 0
	global_load_dwordx4 v[170:173], v150, s[98:99]
	global_load_dwordx4 v[174:177], v150, s[98:99] offset:64
	global_load_dwordx4 v[178:181], v150, s[98:99] offset:512
	global_load_dwordx4 v[182:185], v150, s[98:99] offset:576
	s_add_u32 s98, s98, 0x20000
	s_addc_u32 s99, s99, 0
	global_load_dwordx4 v[186:189], v150, s[98:99]
	global_load_dwordx4 v[190:193], v150, s[98:99] offset:64
	global_load_dwordx4 v[194:197], v150, s[98:99] offset:512
	global_load_dwordx4 v[198:201], v150, s[98:99] offset:576
	s_add_u32 s98, s98, 0x20000
	s_addc_u32 s99, s99, 0
	global_load_dwordx4 v[202:205], v150, s[98:99]
	global_load_dwordx4 v[206:209], v150, s[98:99] offset:64
	global_load_dwordx4 v[210:213], v150, s[98:99] offset:512
	global_load_dwordx4 v[214:217], v150, s[98:99] offset:576
	s_add_u32 s98, s98, 0xa0000
	s_addc_u32 s99, s99, 0
	s_waitcnt vmcnt(15)
	v_pk_add_f32 v[126:127], v[126:127], v[154:155]
	v_pk_add_f32 v[128:129], v[128:129], v[156:157]
	global_store_dwordx4 v150, v[126:129], s[100:101] nt
	global_load_dwordx4 v[154:157], v150, s[98:99]
	s_waitcnt vmcnt(16)
	v_pk_add_f32 v[122:123], v[122:123], v[158:159]
	v_pk_add_f32 v[124:125], v[124:125], v[160:161]
	global_store_dwordx4 v150, v[122:125], s[100:101] offset:64 nt
	global_load_dwordx4 v[158:161], v150, s[98:99] offset:64
	s_waitcnt vmcnt(17)
	v_pk_add_f32 v[118:119], v[118:119], v[162:163]
	v_pk_add_f32 v[120:121], v[120:121], v[164:165]
	global_store_dwordx4 v150, v[118:121], s[100:101] offset:512 nt
	global_load_dwordx4 v[162:165], v150, s[98:99] offset:512
	s_waitcnt vmcnt(18)
	v_pk_add_f32 v[106:107], v[106:107], v[166:167]
	v_pk_add_f32 v[108:109], v[108:109], v[168:169]
	global_store_dwordx4 v150, v[106:109], s[100:101] offset:576 nt
	s_add_u32 s100, s100, 0x20000
	s_addc_u32 s101, s101, 0
	global_load_dwordx4 v[166:169], v150, s[98:99] offset:576
	s_add_u32 s98, s98, 0x20000
	s_addc_u32 s99, s99, 0
	s_waitcnt vmcnt(19)
	v_pk_add_f32 v[114:115], v[114:115], v[170:171]
	v_pk_add_f32 v[116:117], v[116:117], v[172:173]
	global_store_dwordx4 v150, v[114:117], s[100:101] nt
	global_load_dwordx4 v[170:173], v150, s[98:99]
	s_waitcnt vmcnt(20)
	v_pk_add_f32 v[110:111], v[110:111], v[174:175]
	v_pk_add_f32 v[112:113], v[112:113], v[176:177]
	global_store_dwordx4 v150, v[110:113], s[100:101] offset:64 nt
	global_load_dwordx4 v[174:177], v150, s[98:99] offset:64
	s_waitcnt vmcnt(21)
	v_pk_add_f32 v[102:103], v[102:103], v[178:179]
	v_pk_add_f32 v[104:105], v[104:105], v[180:181]
	global_store_dwordx4 v150, v[102:105], s[100:101] offset:512 nt
	global_load_dwordx4 v[178:181], v150, s[98:99] offset:512
	s_waitcnt vmcnt(22)
	v_pk_add_f32 v[90:91], v[90:91], v[182:183]
	v_pk_add_f32 v[92:93], v[92:93], v[184:185]
	global_store_dwordx4 v150, v[90:93], s[100:101] offset:576 nt
	s_add_u32 s100, s100, 0x20000
	s_addc_u32 s101, s101, 0
	global_load_dwordx4 v[182:185], v150, s[98:99] offset:576
	s_add_u32 s98, s98, 0x20000
	s_addc_u32 s99, s99, 0
	s_waitcnt vmcnt(23)
	v_pk_add_f32 v[98:99], v[98:99], v[186:187]
	v_pk_add_f32 v[100:101], v[100:101], v[188:189]
	global_store_dwordx4 v150, v[98:101], s[100:101] nt
	global_load_dwordx4 v[186:189], v150, s[98:99]
	s_waitcnt vmcnt(24)
	v_pk_add_f32 v[94:95], v[94:95], v[190:191]
	v_pk_add_f32 v[96:97], v[96:97], v[192:193]
	global_store_dwordx4 v150, v[94:97], s[100:101] offset:64 nt
	global_load_dwordx4 v[190:193], v150, s[98:99] offset:64
	s_waitcnt vmcnt(25)
	v_pk_add_f32 v[86:87], v[86:87], v[194:195]
	v_pk_add_f32 v[88:89], v[88:89], v[196:197]
	global_store_dwordx4 v150, v[86:89], s[100:101] offset:512 nt
	global_load_dwordx4 v[194:197], v150, s[98:99] offset:512
	s_waitcnt vmcnt(26)
	v_pk_add_f32 v[74:75], v[74:75], v[198:199]
	v_pk_add_f32 v[76:77], v[76:77], v[200:201]
	global_store_dwordx4 v150, v[74:77], s[100:101] offset:576 nt
	s_add_u32 s100, s100, 0x20000
	s_addc_u32 s101, s101, 0
	global_load_dwordx4 v[198:201], v150, s[98:99] offset:576
	s_add_u32 s98, s98, 0x20000
	s_addc_u32 s99, s99, 0
	s_waitcnt vmcnt(27)
	v_pk_add_f32 v[82:83], v[82:83], v[202:203]
	v_pk_add_f32 v[84:85], v[84:85], v[204:205]
	global_store_dwordx4 v150, v[82:85], s[100:101] nt
	global_load_dwordx4 v[202:205], v150, s[98:99]
	s_waitcnt vmcnt(28)
	v_pk_add_f32 v[78:79], v[78:79], v[206:207]
	v_pk_add_f32 v[80:81], v[80:81], v[208:209]
	global_store_dwordx4 v150, v[78:81], s[100:101] offset:64 nt
	global_load_dwordx4 v[206:209], v150, s[98:99] offset:64
	s_waitcnt vmcnt(29)
	v_pk_add_f32 v[70:71], v[70:71], v[210:211]
	v_pk_add_f32 v[72:73], v[72:73], v[212:213]
	global_store_dwordx4 v150, v[70:73], s[100:101] offset:512 nt
	global_load_dwordx4 v[210:213], v150, s[98:99] offset:512
	s_waitcnt vmcnt(30)
	v_pk_add_f32 v[66:67], v[66:67], v[214:215]
	v_pk_add_f32 v[68:69], v[68:69], v[216:217]
	global_store_dwordx4 v150, v[66:69], s[100:101] offset:576 nt
	s_add_u32 s100, s100, 0xa0000
	s_addc_u32 s101, s101, 0
	global_load_dwordx4 v[214:217], v150, s[98:99] offset:576
	s_waitcnt vmcnt(30)
	v_pk_add_f32 v[62:63], v[62:63], v[154:155]
	v_pk_add_f32 v[64:65], v[64:65], v[156:157]
	global_store_dwordx4 v150, v[62:65], s[100:101] nt
	s_waitcnt vmcnt(29)
	v_pk_add_f32 v[58:59], v[58:59], v[158:159]
	v_pk_add_f32 v[60:61], v[60:61], v[160:161]
	global_store_dwordx4 v150, v[58:61], s[100:101] offset:64 nt
	s_waitcnt vmcnt(28)
	v_pk_add_f32 v[54:55], v[54:55], v[162:163]
	v_pk_add_f32 v[56:57], v[56:57], v[164:165]
	global_store_dwordx4 v150, v[54:57], s[100:101] offset:512 nt
	s_waitcnt vmcnt(27)
	v_pk_add_f32 v[42:43], v[42:43], v[166:167]
	v_pk_add_f32 v[44:45], v[44:45], v[168:169]
	global_store_dwordx4 v150, v[42:45], s[100:101] offset:576 nt
	s_add_u32 s100, s100, 0x20000
	s_addc_u32 s101, s101, 0
	s_waitcnt vmcnt(26)
	v_pk_add_f32 v[50:51], v[50:51], v[170:171]
	v_pk_add_f32 v[52:53], v[52:53], v[172:173]
	global_store_dwordx4 v150, v[50:53], s[100:101] nt
	s_waitcnt vmcnt(25)
	v_pk_add_f32 v[46:47], v[46:47], v[174:175]
	v_pk_add_f32 v[48:49], v[48:49], v[176:177]
	global_store_dwordx4 v150, v[46:49], s[100:101] offset:64 nt
	s_waitcnt vmcnt(24)
	v_pk_add_f32 v[38:39], v[38:39], v[178:179]
	v_pk_add_f32 v[40:41], v[40:41], v[180:181]
	global_store_dwordx4 v150, v[38:41], s[100:101] offset:512 nt
	s_waitcnt vmcnt(23)
	v_pk_add_f32 v[26:27], v[26:27], v[182:183]
	v_pk_add_f32 v[28:29], v[28:29], v[184:185]
	global_store_dwordx4 v150, v[26:29], s[100:101] offset:576 nt
	s_add_u32 s100, s100, 0x20000
	s_addc_u32 s101, s101, 0
	s_waitcnt vmcnt(22)
	v_pk_add_f32 v[34:35], v[34:35], v[186:187]
	v_pk_add_f32 v[36:37], v[36:37], v[188:189]
	global_store_dwordx4 v150, v[34:37], s[100:101] nt
	s_waitcnt vmcnt(21)
	v_pk_add_f32 v[30:31], v[30:31], v[190:191]
	v_pk_add_f32 v[32:33], v[32:33], v[192:193]
	global_store_dwordx4 v150, v[30:33], s[100:101] offset:64 nt
	s_waitcnt vmcnt(20)
	v_pk_add_f32 v[22:23], v[22:23], v[194:195]
	v_pk_add_f32 v[24:25], v[24:25], v[196:197]
	global_store_dwordx4 v150, v[22:25], s[100:101] offset:512 nt
	s_waitcnt vmcnt(19)
	v_pk_add_f32 v[10:11], v[10:11], v[198:199]
	v_pk_add_f32 v[12:13], v[12:13], v[200:201]
	global_store_dwordx4 v150, v[10:13], s[100:101] offset:576 nt
	s_add_u32 s100, s100, 0x20000
	s_addc_u32 s101, s101, 0
	s_waitcnt vmcnt(18)
	v_pk_add_f32 v[18:19], v[18:19], v[202:203]
	v_pk_add_f32 v[20:21], v[20:21], v[204:205]
	global_store_dwordx4 v150, v[18:21], s[100:101] nt
	s_waitcnt vmcnt(17)
	v_pk_add_f32 v[14:15], v[14:15], v[206:207]
	v_pk_add_f32 v[16:17], v[16:17], v[208:209]
	global_store_dwordx4 v150, v[14:17], s[100:101] offset:64 nt
	s_waitcnt vmcnt(16)
	v_pk_add_f32 v[6:7], v[6:7], v[210:211]
	v_pk_add_f32 v[8:9], v[8:9], v[212:213]
	global_store_dwordx4 v150, v[6:9], s[100:101] offset:512 nt
	s_waitcnt vmcnt(15)
	v_pk_add_f32 v[2:3], v[2:3], v[214:215]
	v_pk_add_f32 v[4:5], v[4:5], v[216:217]
	global_store_dwordx4 v150, v[2:5], s[100:101] offset:576 nt
	s_cbranch_vccnz .LBB0_1004
	s_andn2_b64 vcc, exec, s[10:11]
	s_cbranch_vccnz .LBB0_989
	s_barrier
	s_branch .LBB0_989

.LBB0_1591:
	s_waitcnt vmcnt(0)
	v_pk_add_f32 v[8:9], v[42:43], v[174:175]
	v_pk_add_f32 v[6:7], v[44:45], v[176:177]
	v_min_f32_e32 v8, 0x40e00000, v8
	v_min_f32_e32 v9, 0x40e00000, v9
	v_pk_mul_f32 v[10:11], v[8:9], s[20:21] op_sel_hi:[1,0]
	v_min_f32_e32 v6, 0x40e00000, v6
	v_exp_f32_e32 v10, v10
	v_exp_f32_e32 v11, v11
	v_min_f32_e32 v7, 0x40e00000, v7
	v_pk_mul_f32 v[16:17], v[6:7], s[20:21] op_sel_hi:[1,0]
	v_pk_add_f32 v[14:15], v[50:51], v[178:179]
	v_pk_add_f32 v[10:11], v[10:11], 1.0 op_sel_hi:[1,0]
	v_exp_f32_e32 v16, v16
	v_rcp_f32_e32 v10, v10
	v_rcp_f32_e32 v11, v11
	v_exp_f32_e32 v17, v17
	v_med3_f32 v14, v14, s53, v212
	v_med3_f32 v15, v15, s53, v212
	v_pk_mul_f32 v[8:9], v[8:9], v[10:11]
	v_pk_fma_f32 v[10:11], v[14:15], 4.0, 4.0 op_sel_hi:[1,0,0]
	v_pk_add_f32 v[14:15], v[16:17], 1.0 op_sel_hi:[1,0]
	v_pk_add_f32 v[12:13], v[52:53], v[180:181]
	v_rcp_f32_e32 v14, v14
	v_rcp_f32_e32 v15, v15
	v_pk_mul_f32 v[8:9], v[8:9], v[10:11]
	v_med3_f32 v10, v12, s53, v212
	v_med3_f32 v11, v13, s53, v212
	v_pk_add_f32 v[12:13], v[38:39], v[166:167]
	v_pk_mul_f32 v[6:7], v[6:7], v[14:15]
	v_min_f32_e32 v12, 0x40e00000, v12
	v_min_f32_e32 v13, 0x40e00000, v13
	v_pk_mul_f32 v[14:15], v[12:13], s[20:21] op_sel_hi:[1,0]
	v_pk_fma_f32 v[10:11], v[10:11], 4.0, 4.0 op_sel_hi:[1,0,0]
	v_exp_f32_e32 v14, v14
	v_exp_f32_e32 v15, v15
	v_pk_mul_f32 v[6:7], v[6:7], v[10:11]
	v_pk_add_f32 v[10:11], v[40:41], v[168:169]
	v_pk_add_f32 v[18:19], v[46:47], v[170:171]
	v_min_f32_e32 v10, 0x40e00000, v10
	v_min_f32_e32 v11, 0x40e00000, v11
	v_pk_add_f32 v[14:15], v[14:15], 1.0 op_sel_hi:[1,0]
	v_pk_mul_f32 v[20:21], v[10:11], s[20:21] op_sel_hi:[1,0]
	v_rcp_f32_e32 v14, v14
	v_rcp_f32_e32 v15, v15
	v_exp_f32_e32 v20, v20
	v_exp_f32_e32 v21, v21
	v_med3_f32 v18, v18, s53, v212
	v_med3_f32 v19, v19, s53, v212
	v_pk_mul_f32 v[12:13], v[12:13], v[14:15]
	v_pk_fma_f32 v[14:15], v[18:19], 4.0, 4.0 op_sel_hi:[1,0,0]
	v_pk_add_f32 v[18:19], v[20:21], 1.0 op_sel_hi:[1,0]
	v_pk_add_f32 v[16:17], v[48:49], v[172:173]
	v_rcp_f32_e32 v18, v18
	v_rcp_f32_e32 v19, v19
	v_pk_mul_f32 v[12:13], v[12:13], v[14:15]
	v_med3_f32 v15, v17, s53, v212
	v_mov_b32_e32 v17, v35
	v_med3_f32 v14, v16, s53, v212
	v_mov_b32_e32 v16, v35
	v_cvt_pk_fp8_f32 v17, v12, v13
	v_cvt_pk_fp8_f32 v16, v8, v9
	v_pk_mul_f32 v[10:11], v[10:11], v[18:19]
	v_pk_fma_f32 v[8:9], v[14:15], 4.0, 4.0 op_sel_hi:[1,0,0]
	v_lshl_add_u32 v4, s56, 8, v205
	v_pk_mul_f32 v[8:9], v[10:11], v[8:9]
	v_cvt_pk_fp8_f32 v16, v6, v7 op_sel:[0,0,1]
	v_cvt_pk_fp8_f32 v17, v8, v9 op_sel:[0,0,1]
	v_pk_add_f32 v[8:9], v[42:43], v[158:159]
	v_mov_b64_e32 v[2:3], s[0:1]
	v_min_f32_e32 v8, 0x40e00000, v8
	v_min_f32_e32 v9, 0x40e00000, v9
	v_pk_mul_f32 v[10:11], v[8:9], s[20:21] op_sel_hi:[1,0]
	v_mad_i64_i32 v[6:7], s[26:27], v4, s52, v[2:3]
	v_exp_f32_e32 v10, v10
	v_exp_f32_e32 v11, v11
	v_lshl_add_u64 v[6:7], v[6:7], 0, v[34:35]
	s_nop 15
	s_nop 15
	global_store_dwordx2 v[6:7], v[16:17], off nt
	v_pk_add_f32 v[6:7], v[44:45], v[160:161]
	v_pk_add_f32 v[10:11], v[10:11], 1.0 op_sel_hi:[1,0]
	v_min_f32_e32 v6, 0x40e00000, v6
	v_min_f32_e32 v7, 0x40e00000, v7
	v_pk_mul_f32 v[16:17], v[6:7], s[20:21] op_sel_hi:[1,0]
	v_rcp_f32_e32 v10, v10
	v_rcp_f32_e32 v11, v11
	v_exp_f32_e32 v16, v16
	v_exp_f32_e32 v17, v17
	v_pk_add_f32 v[14:15], v[50:51], v[162:163]
	v_pk_mul_f32 v[8:9], v[8:9], v[10:11]
	v_med3_f32 v14, v14, s53, v212
	v_med3_f32 v15, v15, s53, v212
	v_pk_fma_f32 v[10:11], v[14:15], 4.0, 4.0 op_sel_hi:[1,0,0]
	v_pk_add_f32 v[14:15], v[16:17], 1.0 op_sel_hi:[1,0]
	v_pk_add_f32 v[12:13], v[52:53], v[164:165]
	v_rcp_f32_e32 v14, v14
	v_rcp_f32_e32 v15, v15
	v_pk_mul_f32 v[8:9], v[8:9], v[10:11]
	v_med3_f32 v10, v12, s53, v212
	v_med3_f32 v11, v13, s53, v212
	v_pk_add_f32 v[12:13], v[38:39], v[150:151]
	v_pk_mul_f32 v[6:7], v[6:7], v[14:15]
	v_min_f32_e32 v12, 0x40e00000, v12
	v_min_f32_e32 v13, 0x40e00000, v13
	v_pk_mul_f32 v[14:15], v[12:13], s[20:21] op_sel_hi:[1,0]
	v_pk_fma_f32 v[10:11], v[10:11], 4.0, 4.0 op_sel_hi:[1,0,0]
	v_exp_f32_e32 v14, v14
	v_exp_f32_e32 v15, v15
	v_pk_mul_f32 v[6:7], v[6:7], v[10:11]
	v_pk_add_f32 v[10:11], v[40:41], v[152:153]
	v_pk_add_f32 v[18:19], v[46:47], v[154:155]
	v_min_f32_e32 v10, 0x40e00000, v10
	v_min_f32_e32 v11, 0x40e00000, v11
	v_pk_add_f32 v[14:15], v[14:15], 1.0 op_sel_hi:[1,0]
	v_pk_mul_f32 v[20:21], v[10:11], s[20:21] op_sel_hi:[1,0]
	v_rcp_f32_e32 v14, v14
	v_rcp_f32_e32 v15, v15
	v_exp_f32_e32 v20, v20
	v_exp_f32_e32 v21, v21
	v_med3_f32 v18, v18, s53, v212
	v_med3_f32 v19, v19, s53, v212
	v_pk_mul_f32 v[12:13], v[12:13], v[14:15]
	v_pk_fma_f32 v[14:15], v[18:19], 4.0, 4.0 op_sel_hi:[1,0,0]
	v_pk_add_f32 v[18:19], v[20:21], 1.0 op_sel_hi:[1,0]
	v_pk_add_f32 v[16:17], v[48:49], v[156:157]
	v_rcp_f32_e32 v18, v18
	v_rcp_f32_e32 v19, v19
	v_pk_mul_f32 v[12:13], v[12:13], v[14:15]
	v_med3_f32 v15, v17, s53, v212
	v_mov_b32_e32 v17, v35
	v_med3_f32 v14, v16, s53, v212
	v_mov_b32_e32 v16, v35
	v_cvt_pk_fp8_f32 v17, v12, v13
	v_cvt_pk_fp8_f32 v16, v8, v9
	v_pk_mul_f32 v[10:11], v[10:11], v[18:19]
	v_pk_fma_f32 v[8:9], v[14:15], 4.0, 4.0 op_sel_hi:[1,0,0]
	v_or_b32_e32 v5, 16, v4
	v_pk_mul_f32 v[8:9], v[10:11], v[8:9]
	v_cvt_pk_fp8_f32 v16, v6, v7 op_sel:[0,0,1]
	v_cvt_pk_fp8_f32 v17, v8, v9 op_sel:[0,0,1]
	v_pk_add_f32 v[8:9], v[42:43], v[142:143]
	v_mad_i64_i32 v[6:7], s[26:27], v5, s52, v[2:3]
	v_min_f32_e32 v8, 0x40e00000, v8
	v_min_f32_e32 v9, 0x40e00000, v9
	v_pk_mul_f32 v[10:11], v[8:9], s[20:21] op_sel_hi:[1,0]
	v_lshl_add_u64 v[6:7], v[6:7], 0, v[34:35]
	v_exp_f32_e32 v10, v10
	v_exp_f32_e32 v11, v11
	global_store_dwordx2 v[6:7], v[16:17], off nt
	v_pk_add_f32 v[6:7], v[44:45], v[144:145]
	v_pk_add_f32 v[14:15], v[50:51], v[146:147]
	v_min_f32_e32 v6, 0x40e00000, v6
	v_min_f32_e32 v7, 0x40e00000, v7
	v_pk_add_f32 v[10:11], v[10:11], 1.0 op_sel_hi:[1,0]
	v_pk_mul_f32 v[16:17], v[6:7], s[20:21] op_sel_hi:[1,0]
	v_rcp_f32_e32 v10, v10
	v_rcp_f32_e32 v11, v11
	v_exp_f32_e32 v16, v16
	v_exp_f32_e32 v17, v17
	v_med3_f32 v14, v14, s53, v212
	v_med3_f32 v15, v15, s53, v212
	v_pk_mul_f32 v[8:9], v[8:9], v[10:11]
	v_pk_fma_f32 v[10:11], v[14:15], 4.0, 4.0 op_sel_hi:[1,0,0]
	v_pk_add_f32 v[14:15], v[16:17], 1.0 op_sel_hi:[1,0]
	v_pk_add_f32 v[12:13], v[52:53], v[148:149]
	v_rcp_f32_e32 v14, v14
	v_rcp_f32_e32 v15, v15
	v_pk_mul_f32 v[8:9], v[8:9], v[10:11]
	v_med3_f32 v10, v12, s53, v212
	v_med3_f32 v11, v13, s53, v212
	v_pk_add_f32 v[12:13], v[38:39], v[134:135]
	v_pk_mul_f32 v[6:7], v[6:7], v[14:15]
	v_min_f32_e32 v12, 0x40e00000, v12
	v_min_f32_e32 v13, 0x40e00000, v13
	v_pk_mul_f32 v[14:15], v[12:13], s[20:21] op_sel_hi:[1,0]
	v_pk_fma_f32 v[10:11], v[10:11], 4.0, 4.0 op_sel_hi:[1,0,0]
	v_exp_f32_e32 v14, v14
	v_exp_f32_e32 v15, v15
	v_pk_mul_f32 v[6:7], v[6:7], v[10:11]
	v_pk_add_f32 v[10:11], v[40:41], v[136:137]
	v_pk_add_f32 v[18:19], v[46:47], v[138:139]
	v_min_f32_e32 v10, 0x40e00000, v10
	v_min_f32_e32 v11, 0x40e00000, v11
	v_pk_add_f32 v[14:15], v[14:15], 1.0 op_sel_hi:[1,0]
	v_pk_mul_f32 v[20:21], v[10:11], s[20:21] op_sel_hi:[1,0]
	v_rcp_f32_e32 v14, v14
	v_rcp_f32_e32 v15, v15
	v_exp_f32_e32 v20, v20
	v_exp_f32_e32 v21, v21
	v_med3_f32 v18, v18, s53, v212
	v_med3_f32 v19, v19, s53, v212
	v_pk_mul_f32 v[12:13], v[12:13], v[14:15]
	v_pk_fma_f32 v[14:15], v[18:19], 4.0, 4.0 op_sel_hi:[1,0,0]
	v_pk_add_f32 v[18:19], v[20:21], 1.0 op_sel_hi:[1,0]
	v_pk_add_f32 v[16:17], v[48:49], v[140:141]
	v_rcp_f32_e32 v18, v18
	v_rcp_f32_e32 v19, v19
	v_pk_mul_f32 v[12:13], v[12:13], v[14:15]
	v_med3_f32 v15, v17, s53, v212
	v_mov_b32_e32 v17, v35
	v_med3_f32 v14, v16, s53, v212
	v_mov_b32_e32 v16, v35
	v_cvt_pk_fp8_f32 v17, v12, v13
	v_cvt_pk_fp8_f32 v16, v8, v9
	v_pk_mul_f32 v[10:11], v[10:11], v[18:19]
	v_pk_fma_f32 v[8:9], v[14:15], 4.0, 4.0 op_sel_hi:[1,0,0]
	v_or_b32_e32 v5, 32, v4
	v_pk_mul_f32 v[8:9], v[10:11], v[8:9]
	v_cvt_pk_fp8_f32 v16, v6, v7 op_sel:[0,0,1]
	v_cvt_pk_fp8_f32 v17, v8, v9 op_sel:[0,0,1]
	v_pk_add_f32 v[8:9], v[42:43], v[126:127]
	v_mad_i64_i32 v[6:7], s[26:27], v5, s52, v[2:3]
	v_min_f32_e32 v8, 0x40e00000, v8
	v_min_f32_e32 v9, 0x40e00000, v9
	v_pk_mul_f32 v[10:11], v[8:9], s[20:21] op_sel_hi:[1,0]
	v_lshl_add_u64 v[6:7], v[6:7], 0, v[34:35]
	v_exp_f32_e32 v10, v10
	v_exp_f32_e32 v11, v11
	global_store_dwordx2 v[6:7], v[16:17], off nt
	v_pk_add_f32 v[6:7], v[44:45], v[128:129]
	v_pk_add_f32 v[14:15], v[50:51], v[130:131]
	v_min_f32_e32 v6, 0x40e00000, v6
	v_min_f32_e32 v7, 0x40e00000, v7
	v_pk_add_f32 v[10:11], v[10:11], 1.0 op_sel_hi:[1,0]
	v_pk_mul_f32 v[16:17], v[6:7], s[20:21] op_sel_hi:[1,0]
	v_rcp_f32_e32 v10, v10
	v_rcp_f32_e32 v11, v11
	v_exp_f32_e32 v16, v16
	v_exp_f32_e32 v17, v17
	v_med3_f32 v14, v14, s53, v212
	v_med3_f32 v15, v15, s53, v212
	v_pk_mul_f32 v[8:9], v[8:9], v[10:11]
	v_pk_fma_f32 v[10:11], v[14:15], 4.0, 4.0 op_sel_hi:[1,0,0]
	v_pk_add_f32 v[14:15], v[16:17], 1.0 op_sel_hi:[1,0]
	v_pk_add_f32 v[12:13], v[52:53], v[132:133]
	v_rcp_f32_e32 v14, v14
	v_rcp_f32_e32 v15, v15
	v_pk_mul_f32 v[8:9], v[8:9], v[10:11]
	v_med3_f32 v10, v12, s53, v212
	v_med3_f32 v11, v13, s53, v212
	v_pk_add_f32 v[12:13], v[38:39], v[110:111]
	v_pk_mul_f32 v[6:7], v[6:7], v[14:15]
	v_min_f32_e32 v12, 0x40e00000, v12
	v_min_f32_e32 v13, 0x40e00000, v13
	v_pk_mul_f32 v[14:15], v[12:13], s[20:21] op_sel_hi:[1,0]
	v_pk_fma_f32 v[10:11], v[10:11], 4.0, 4.0 op_sel_hi:[1,0,0]
	v_exp_f32_e32 v14, v14
	v_exp_f32_e32 v15, v15
	v_pk_mul_f32 v[6:7], v[6:7], v[10:11]
	v_pk_add_f32 v[10:11], v[40:41], v[112:113]
	v_pk_add_f32 v[18:19], v[46:47], v[118:119]
	v_min_f32_e32 v10, 0x40e00000, v10
	v_min_f32_e32 v11, 0x40e00000, v11
	v_pk_add_f32 v[14:15], v[14:15], 1.0 op_sel_hi:[1,0]
	v_pk_mul_f32 v[20:21], v[10:11], s[20:21] op_sel_hi:[1,0]
	v_rcp_f32_e32 v14, v14
	v_rcp_f32_e32 v15, v15
	v_exp_f32_e32 v20, v20
	v_exp_f32_e32 v21, v21
	v_med3_f32 v18, v18, s53, v212
	v_med3_f32 v19, v19, s53, v212
	v_pk_mul_f32 v[12:13], v[12:13], v[14:15]
	v_pk_fma_f32 v[14:15], v[18:19], 4.0, 4.0 op_sel_hi:[1,0,0]
	v_pk_add_f32 v[18:19], v[20:21], 1.0 op_sel_hi:[1,0]
	v_pk_add_f32 v[16:17], v[48:49], v[120:121]
	v_rcp_f32_e32 v18, v18
	v_rcp_f32_e32 v19, v19
	v_pk_mul_f32 v[12:13], v[12:13], v[14:15]
	v_med3_f32 v15, v17, s53, v212
	v_mov_b32_e32 v17, v35
	v_med3_f32 v14, v16, s53, v212
	v_mov_b32_e32 v16, v35
	v_cvt_pk_fp8_f32 v17, v12, v13
	v_cvt_pk_fp8_f32 v16, v8, v9
	v_pk_mul_f32 v[10:11], v[10:11], v[18:19]
	v_pk_fma_f32 v[8:9], v[14:15], 4.0, 4.0 op_sel_hi:[1,0,0]
	v_or_b32_e32 v5, 48, v4
	v_pk_mul_f32 v[8:9], v[10:11], v[8:9]
	v_cvt_pk_fp8_f32 v16, v6, v7 op_sel:[0,0,1]
	v_cvt_pk_fp8_f32 v17, v8, v9 op_sel:[0,0,1]
	v_pk_add_f32 v[8:9], v[42:43], v[114:115]
	v_mad_i64_i32 v[6:7], s[26:27], v5, s52, v[2:3]
	v_min_f32_e32 v8, 0x40e00000, v8
	v_min_f32_e32 v9, 0x40e00000, v9
	v_pk_mul_f32 v[10:11], v[8:9], s[20:21] op_sel_hi:[1,0]
	v_lshl_add_u64 v[6:7], v[6:7], 0, v[34:35]
	v_exp_f32_e32 v10, v10
	v_exp_f32_e32 v11, v11
	global_store_dwordx2 v[6:7], v[16:17], off nt
	v_pk_add_f32 v[6:7], v[44:45], v[116:117]
	v_pk_add_f32 v[14:15], v[50:51], v[122:123]
	v_min_f32_e32 v6, 0x40e00000, v6
	v_min_f32_e32 v7, 0x40e00000, v7
	v_pk_add_f32 v[10:11], v[10:11], 1.0 op_sel_hi:[1,0]
	v_pk_mul_f32 v[16:17], v[6:7], s[20:21] op_sel_hi:[1,0]
	v_rcp_f32_e32 v10, v10
	v_rcp_f32_e32 v11, v11
	v_exp_f32_e32 v16, v16
	v_exp_f32_e32 v17, v17
	v_med3_f32 v14, v14, s53, v212
	v_med3_f32 v15, v15, s53, v212
	v_pk_mul_f32 v[8:9], v[8:9], v[10:11]
	v_pk_fma_f32 v[10:11], v[14:15], 4.0, 4.0 op_sel_hi:[1,0,0]
	v_pk_add_f32 v[14:15], v[16:17], 1.0 op_sel_hi:[1,0]
	v_pk_add_f32 v[12:13], v[52:53], v[124:125]
	v_rcp_f32_e32 v14, v14
	v_rcp_f32_e32 v15, v15
	v_pk_mul_f32 v[8:9], v[8:9], v[10:11]
	v_med3_f32 v10, v12, s53, v212
	v_med3_f32 v11, v13, s53, v212
	v_pk_add_f32 v[12:13], v[38:39], v[102:103]
	v_pk_mul_f32 v[6:7], v[6:7], v[14:15]
	v_min_f32_e32 v12, 0x40e00000, v12
	v_min_f32_e32 v13, 0x40e00000, v13
	v_pk_mul_f32 v[14:15], v[12:13], s[20:21] op_sel_hi:[1,0]
	v_pk_fma_f32 v[10:11], v[10:11], 4.0, 4.0 op_sel_hi:[1,0,0]
	v_exp_f32_e32 v14, v14
	v_exp_f32_e32 v15, v15
	v_pk_mul_f32 v[6:7], v[6:7], v[10:11]
	v_pk_add_f32 v[10:11], v[40:41], v[104:105]
	v_pk_add_f32 v[18:19], v[46:47], v[106:107]
	v_min_f32_e32 v10, 0x40e00000, v10
	v_min_f32_e32 v11, 0x40e00000, v11
	v_pk_add_f32 v[14:15], v[14:15], 1.0 op_sel_hi:[1,0]
	v_pk_mul_f32 v[20:21], v[10:11], s[20:21] op_sel_hi:[1,0]
	v_rcp_f32_e32 v14, v14
	v_rcp_f32_e32 v15, v15
	v_exp_f32_e32 v20, v20
	v_exp_f32_e32 v21, v21
	v_med3_f32 v18, v18, s53, v212
	v_med3_f32 v19, v19, s53, v212
	v_pk_mul_f32 v[12:13], v[12:13], v[14:15]
	v_pk_fma_f32 v[14:15], v[18:19], 4.0, 4.0 op_sel_hi:[1,0,0]
	v_pk_add_f32 v[18:19], v[20:21], 1.0 op_sel_hi:[1,0]
	v_pk_add_f32 v[16:17], v[48:49], v[108:109]
	v_rcp_f32_e32 v18, v18
	v_rcp_f32_e32 v19, v19
	v_pk_mul_f32 v[12:13], v[12:13], v[14:15]
	v_med3_f32 v15, v17, s53, v212
	v_mov_b32_e32 v17, v35
	v_med3_f32 v14, v16, s53, v212
	v_mov_b32_e32 v16, v35
	v_cvt_pk_fp8_f32 v17, v12, v13
	v_cvt_pk_fp8_f32 v16, v8, v9
	v_pk_mul_f32 v[10:11], v[10:11], v[18:19]
	v_pk_fma_f32 v[8:9], v[14:15], 4.0, 4.0 op_sel_hi:[1,0,0]
	v_add_u32_e32 v5, 0x80, v4
	v_pk_mul_f32 v[8:9], v[10:11], v[8:9]
	v_cvt_pk_fp8_f32 v16, v6, v7 op_sel:[0,0,1]
	v_cvt_pk_fp8_f32 v17, v8, v9 op_sel:[0,0,1]
	v_pk_add_f32 v[8:9], v[42:43], v[94:95]
	v_mad_i64_i32 v[6:7], s[26:27], v5, s52, v[2:3]
	v_min_f32_e32 v8, 0x40e00000, v8
	v_min_f32_e32 v9, 0x40e00000, v9
	v_pk_mul_f32 v[10:11], v[8:9], s[20:21] op_sel_hi:[1,0]
	v_lshl_add_u64 v[6:7], v[6:7], 0, v[34:35]
	v_exp_f32_e32 v10, v10
	v_exp_f32_e32 v11, v11
	global_store_dwordx2 v[6:7], v[16:17], off nt
	v_pk_add_f32 v[6:7], v[44:45], v[96:97]
	v_pk_add_f32 v[14:15], v[50:51], v[98:99]
	v_min_f32_e32 v6, 0x40e00000, v6
	v_min_f32_e32 v7, 0x40e00000, v7
	v_pk_add_f32 v[10:11], v[10:11], 1.0 op_sel_hi:[1,0]
	v_pk_mul_f32 v[16:17], v[6:7], s[20:21] op_sel_hi:[1,0]
	v_rcp_f32_e32 v10, v10
	v_rcp_f32_e32 v11, v11
	v_exp_f32_e32 v16, v16
	v_exp_f32_e32 v17, v17
	v_med3_f32 v14, v14, s53, v212
	v_med3_f32 v15, v15, s53, v212
	v_pk_mul_f32 v[8:9], v[8:9], v[10:11]
	v_pk_fma_f32 v[10:11], v[14:15], 4.0, 4.0 op_sel_hi:[1,0,0]
	v_pk_add_f32 v[14:15], v[16:17], 1.0 op_sel_hi:[1,0]
	v_pk_add_f32 v[12:13], v[52:53], v[100:101]
	v_rcp_f32_e32 v14, v14
	v_rcp_f32_e32 v15, v15
	v_pk_mul_f32 v[8:9], v[8:9], v[10:11]
	v_med3_f32 v10, v12, s53, v212
	v_med3_f32 v11, v13, s53, v212
	v_pk_add_f32 v[12:13], v[38:39], v[86:87]
	v_pk_mul_f32 v[6:7], v[6:7], v[14:15]
	v_min_f32_e32 v12, 0x40e00000, v12
	v_min_f32_e32 v13, 0x40e00000, v13
	v_pk_mul_f32 v[14:15], v[12:13], s[20:21] op_sel_hi:[1,0]
	v_pk_fma_f32 v[10:11], v[10:11], 4.0, 4.0 op_sel_hi:[1,0,0]
	v_exp_f32_e32 v14, v14
	v_exp_f32_e32 v15, v15
	v_pk_mul_f32 v[6:7], v[6:7], v[10:11]
	v_pk_add_f32 v[10:11], v[40:41], v[88:89]
	v_pk_add_f32 v[18:19], v[46:47], v[90:91]
	v_min_f32_e32 v10, 0x40e00000, v10
	v_min_f32_e32 v11, 0x40e00000, v11
	v_pk_add_f32 v[14:15], v[14:15], 1.0 op_sel_hi:[1,0]
	v_pk_mul_f32 v[20:21], v[10:11], s[20:21] op_sel_hi:[1,0]
	v_rcp_f32_e32 v14, v14
	v_rcp_f32_e32 v15, v15
	v_exp_f32_e32 v20, v20
	v_exp_f32_e32 v21, v21
	v_med3_f32 v18, v18, s53, v212
	v_med3_f32 v19, v19, s53, v212
	v_pk_mul_f32 v[12:13], v[12:13], v[14:15]
	v_pk_fma_f32 v[14:15], v[18:19], 4.0, 4.0 op_sel_hi:[1,0,0]
	v_pk_add_f32 v[18:19], v[20:21], 1.0 op_sel_hi:[1,0]
	v_pk_add_f32 v[16:17], v[48:49], v[92:93]
	v_rcp_f32_e32 v18, v18
	v_rcp_f32_e32 v19, v19
	v_pk_mul_f32 v[12:13], v[12:13], v[14:15]
	v_med3_f32 v15, v17, s53, v212
	v_mov_b32_e32 v17, v35
	v_med3_f32 v14, v16, s53, v212
	v_mov_b32_e32 v16, v35
	v_cvt_pk_fp8_f32 v17, v12, v13
	v_cvt_pk_fp8_f32 v16, v8, v9
	v_pk_mul_f32 v[10:11], v[10:11], v[18:19]
	v_pk_fma_f32 v[8:9], v[14:15], 4.0, 4.0 op_sel_hi:[1,0,0]
	v_add_u32_e32 v5, 0x90, v4
	v_pk_mul_f32 v[8:9], v[10:11], v[8:9]
	v_cvt_pk_fp8_f32 v16, v6, v7 op_sel:[0,0,1]
	v_cvt_pk_fp8_f32 v17, v8, v9 op_sel:[0,0,1]
	v_pk_add_f32 v[8:9], v[42:43], v[78:79]
	v_mad_i64_i32 v[6:7], s[26:27], v5, s52, v[2:3]
	v_min_f32_e32 v8, 0x40e00000, v8
	v_min_f32_e32 v9, 0x40e00000, v9
	v_pk_mul_f32 v[10:11], v[8:9], s[20:21] op_sel_hi:[1,0]
	v_lshl_add_u64 v[6:7], v[6:7], 0, v[34:35]
	v_exp_f32_e32 v10, v10
	v_exp_f32_e32 v11, v11
	global_store_dwordx2 v[6:7], v[16:17], off nt
	v_pk_add_f32 v[6:7], v[44:45], v[80:81]
	v_pk_add_f32 v[14:15], v[50:51], v[82:83]
	v_min_f32_e32 v6, 0x40e00000, v6
	v_min_f32_e32 v7, 0x40e00000, v7
	v_pk_add_f32 v[10:11], v[10:11], 1.0 op_sel_hi:[1,0]
	v_pk_mul_f32 v[16:17], v[6:7], s[20:21] op_sel_hi:[1,0]
	v_rcp_f32_e32 v10, v10
	v_rcp_f32_e32 v11, v11
	v_exp_f32_e32 v16, v16
	v_exp_f32_e32 v17, v17
	v_med3_f32 v14, v14, s53, v212
	v_med3_f32 v15, v15, s53, v212
	v_pk_mul_f32 v[8:9], v[8:9], v[10:11]
	v_pk_fma_f32 v[10:11], v[14:15], 4.0, 4.0 op_sel_hi:[1,0,0]
	v_pk_add_f32 v[14:15], v[16:17], 1.0 op_sel_hi:[1,0]
	v_pk_add_f32 v[12:13], v[52:53], v[84:85]
	v_rcp_f32_e32 v14, v14
	v_rcp_f32_e32 v15, v15
	v_pk_mul_f32 v[8:9], v[8:9], v[10:11]
	v_med3_f32 v10, v12, s53, v212
	v_med3_f32 v11, v13, s53, v212
	v_pk_add_f32 v[12:13], v[38:39], v[70:71]
	v_pk_mul_f32 v[6:7], v[6:7], v[14:15]
	v_min_f32_e32 v12, 0x40e00000, v12
	v_min_f32_e32 v13, 0x40e00000, v13
	v_pk_mul_f32 v[14:15], v[12:13], s[20:21] op_sel_hi:[1,0]
	v_pk_fma_f32 v[10:11], v[10:11], 4.0, 4.0 op_sel_hi:[1,0,0]
	v_exp_f32_e32 v14, v14
	v_exp_f32_e32 v15, v15
	v_pk_mul_f32 v[6:7], v[6:7], v[10:11]
	v_pk_add_f32 v[10:11], v[40:41], v[72:73]
	v_pk_add_f32 v[18:19], v[46:47], v[74:75]
	v_min_f32_e32 v10, 0x40e00000, v10
	v_min_f32_e32 v11, 0x40e00000, v11
	v_pk_add_f32 v[14:15], v[14:15], 1.0 op_sel_hi:[1,0]
	v_pk_mul_f32 v[20:21], v[10:11], s[20:21] op_sel_hi:[1,0]
	v_rcp_f32_e32 v14, v14
	v_rcp_f32_e32 v15, v15
	v_exp_f32_e32 v20, v20
	v_exp_f32_e32 v21, v21
	v_med3_f32 v18, v18, s53, v212
	v_med3_f32 v19, v19, s53, v212
	v_pk_mul_f32 v[12:13], v[12:13], v[14:15]
	v_pk_fma_f32 v[14:15], v[18:19], 4.0, 4.0 op_sel_hi:[1,0,0]
	v_pk_add_f32 v[18:19], v[20:21], 1.0 op_sel_hi:[1,0]
	v_pk_add_f32 v[16:17], v[48:49], v[76:77]
	v_rcp_f32_e32 v18, v18
	v_rcp_f32_e32 v19, v19
	v_pk_mul_f32 v[12:13], v[12:13], v[14:15]
	v_med3_f32 v14, v16, s53, v212
	v_med3_f32 v15, v17, s53, v212
	v_mov_b32_e32 v16, v35
	v_mov_b32_e32 v17, v35
	v_cvt_pk_fp8_f32 v16, v8, v9
	v_cvt_pk_fp8_f32 v17, v12, v13
	v_pk_mul_f32 v[10:11], v[10:11], v[18:19]
	v_pk_fma_f32 v[8:9], v[14:15], 4.0, 4.0 op_sel_hi:[1,0,0]
	v_cvt_pk_fp8_f32 v16, v6, v7 op_sel:[0,0,1]
	v_pk_mul_f32 v[8:9], v[10:11], v[8:9]
	v_add_u32_e32 v5, 0xa0, v4
	v_cvt_pk_fp8_f32 v17, v8, v9 op_sel:[0,0,1]
	v_mad_i64_i32 v[6:7], s[26:27], v5, s52, v[2:3]
	v_lshl_add_u64 v[6:7], v[6:7], 0, v[34:35]
	global_store_dwordx2 v[6:7], v[16:17], off nt
	v_pk_add_f32 v[6:7], v[42:43], v[66:67]
	v_add_u32_e32 v20, 0xb0, v4
	v_min_f32_e32 v6, 0x40e00000, v6
	v_min_f32_e32 v7, 0x40e00000, v7
	v_pk_mul_f32 v[8:9], v[6:7], s[20:21] op_sel_hi:[1,0]
	v_pk_add_f32 v[4:5], v[44:45], v[68:69]
	v_exp_f32_e32 v8, v8
	v_exp_f32_e32 v9, v9
	v_min_f32_e32 v4, 0x40e00000, v4
	v_min_f32_e32 v5, 0x40e00000, v5
	v_pk_mul_f32 v[14:15], v[4:5], s[20:21] op_sel_hi:[1,0]
	v_pk_add_f32 v[8:9], v[8:9], 1.0 op_sel_hi:[1,0]
	v_exp_f32_e32 v14, v14
	v_rcp_f32_e32 v8, v8
	v_rcp_f32_e32 v9, v9
	v_exp_f32_e32 v15, v15
	v_pk_add_f32 v[12:13], v[50:51], v[62:63]
	v_pk_add_f32 v[10:11], v[52:53], v[64:65]
	v_med3_f32 v12, v12, s53, v212
	v_med3_f32 v13, v13, s53, v212
	v_pk_mul_f32 v[6:7], v[6:7], v[8:9]
	v_pk_fma_f32 v[8:9], v[12:13], 4.0, 4.0 op_sel_hi:[1,0,0]
	v_pk_add_f32 v[12:13], v[14:15], 1.0 op_sel_hi:[1,0]
	v_pk_mul_f32 v[6:7], v[6:7], v[8:9]
	v_rcp_f32_e32 v12, v12
	v_rcp_f32_e32 v13, v13
	v_med3_f32 v8, v10, s53, v212
	v_med3_f32 v9, v11, s53, v212
	v_pk_add_f32 v[10:11], v[38:39], v[58:59]
	v_pk_mul_f32 v[4:5], v[4:5], v[12:13]
	v_min_f32_e32 v10, 0x40e00000, v10
	v_min_f32_e32 v11, 0x40e00000, v11
	v_pk_mul_f32 v[12:13], v[10:11], s[20:21] op_sel_hi:[1,0]
	v_pk_fma_f32 v[8:9], v[8:9], 4.0, 4.0 op_sel_hi:[1,0,0]
	v_exp_f32_e32 v12, v12
	v_exp_f32_e32 v13, v13
	v_pk_mul_f32 v[4:5], v[4:5], v[8:9]
	v_pk_add_f32 v[8:9], v[40:41], v[60:61]
	v_pk_add_f32 v[16:17], v[46:47], v[54:55]
	v_min_f32_e32 v8, 0x40e00000, v8
	v_min_f32_e32 v9, 0x40e00000, v9
	v_pk_add_f32 v[12:13], v[12:13], 1.0 op_sel_hi:[1,0]
	v_pk_mul_f32 v[18:19], v[8:9], s[20:21] op_sel_hi:[1,0]
	v_rcp_f32_e32 v12, v12
	v_rcp_f32_e32 v13, v13
	v_exp_f32_e32 v18, v18
	v_exp_f32_e32 v19, v19
	v_med3_f32 v16, v16, s53, v212
	v_med3_f32 v17, v17, s53, v212
	v_pk_mul_f32 v[10:11], v[10:11], v[12:13]
	v_pk_fma_f32 v[12:13], v[16:17], 4.0, 4.0 op_sel_hi:[1,0,0]
	v_pk_add_f32 v[16:17], v[18:19], 1.0 op_sel_hi:[1,0]
	v_pk_add_f32 v[14:15], v[48:49], v[56:57]
	v_rcp_f32_e32 v16, v16
	v_rcp_f32_e32 v17, v17
	v_pk_mul_f32 v[10:11], v[10:11], v[12:13]
	v_med3_f32 v12, v14, s53, v212
	v_med3_f32 v13, v15, s53, v212
	v_mov_b32_e32 v14, v35
	v_mov_b32_e32 v15, v35
	v_cvt_pk_fp8_f32 v14, v6, v7
	v_cvt_pk_fp8_f32 v15, v10, v11
	v_pk_mul_f32 v[8:9], v[8:9], v[16:17]
	v_pk_fma_f32 v[6:7], v[12:13], 4.0, 4.0 op_sel_hi:[1,0,0]
	v_cvt_pk_fp8_f32 v14, v4, v5 op_sel:[0,0,1]
	v_pk_mul_f32 v[6:7], v[8:9], v[6:7]
	v_mad_i64_i32 v[2:3], s[26:27], v20, s52, v[2:3]
	v_cvt_pk_fp8_f32 v15, v6, v7 op_sel:[0,0,1]
	v_lshl_add_u64 v[2:3], v[2:3], 0, v[34:35]
	s_and_b64 vcc, exec, s[2:3]
	global_store_dwordx2 v[2:3], v[14:15], off nt
	s_cbranch_vccnz .LBB0_1594
	s_andn2_b64 vcc, exec, s[10:11]
	s_cbranch_vccnz .LBB0_1577
	s_barrier
	s_branch .LBB0_1577

.LBB0_1673:
	s_waitcnt vmcnt(0)
	v_pk_mul_f32 v[14:15], v[40:41], s[18:19] op_sel_hi:[1,0]
	v_lshl_add_u32 v18, s95, 8, v202
	v_pk_mul_f32 v[10:11], v[42:43], s[18:19] op_sel_hi:[1,0]
	v_ashrrev_i32_e32 v19, 31, v18
	v_pk_fma_f32 v[20:21], v[164:165], s[18:19], v[14:15] op_sel_hi:[1,0,1]
	v_pk_mul_f32 v[12:13], v[36:37], s[18:19] op_sel_hi:[1,0]
	v_lshlrev_b64 v[16:17], 11, v[18:19]
	v_med3_f32 v19, v20, s87, v209
	v_med3_f32 v23, v21, s87, v209
	v_pk_fma_f32 v[20:21], v[166:167], s[18:19], v[10:11] op_sel_hi:[1,0,1]
	v_mov_b32_e32 v22, v33
	v_med3_f32 v24, v20, s87, v209
	v_med3_f32 v25, v21, s87, v209
	v_pk_fma_f32 v[20:21], v[168:169], s[18:19], v[12:13] op_sel_hi:[1,0,1]
	v_cvt_pk_fp8_f32 v22, v19, v23
	v_med3_f32 v26, v20, s87, v209
	v_med3_f32 v27, v21, s87, v209
	v_mov_b32_e32 v23, v33
	v_cvt_pk_fp8_f32 v23, v26, v27
	v_pk_mul_f32 v[8:9], v[38:39], s[18:19] op_sel_hi:[1,0]
	v_pk_mul_f32 v[6:7], v[48:49], s[18:19] op_sel_hi:[1,0]
	v_pk_fma_f32 v[20:21], v[170:171], s[18:19], v[8:9] op_sel_hi:[1,0,1]
	v_pk_mul_f32 v[2:3], v[50:51], s[18:19] op_sel_hi:[1,0]
	v_med3_f32 v19, v20, s87, v209
	v_med3_f32 v20, v21, s87, v209
	v_cvt_pk_fp8_f32 v23, v19, v20 op_sel:[0,0,1]
	v_pk_fma_f32 v[20:21], v[172:173], s[18:19], v[6:7] op_sel_hi:[1,0,1]
	v_pk_mul_f32 v[4:5], v[44:45], s[18:19] op_sel_hi:[1,0]
	v_cvt_pk_fp8_f32 v22, v24, v25 op_sel:[0,0,1]
	v_med3_f32 v19, v20, s87, v209
	v_med3_f32 v25, v21, s87, v209
	v_pk_fma_f32 v[20:21], v[174:175], s[18:19], v[2:3] op_sel_hi:[1,0,1]
	v_mov_b32_e32 v24, v33
	v_med3_f32 v26, v20, s87, v209
	v_med3_f32 v27, v21, s87, v209
	v_pk_fma_f32 v[20:21], v[176:177], s[18:19], v[4:5] op_sel_hi:[1,0,1]
	v_cvt_pk_fp8_f32 v24, v19, v25
	v_med3_f32 v28, v20, s87, v209
	v_med3_f32 v29, v21, s87, v209
	v_mov_b32_e32 v25, v33
	v_cvt_pk_fp8_f32 v25, v28, v29
	v_pk_mul_f32 v[0:1], v[46:47], s[18:19] op_sel_hi:[1,0]
	v_cvt_pk_fp8_f32 v24, v26, v27 op_sel:[0,0,1]
	v_pk_fma_f32 v[20:21], v[178:179], s[18:19], v[0:1] op_sel_hi:[1,0,1]
	v_lshl_add_u64 v[16:17], s[4:5], 0, v[16:17]
	v_med3_f32 v19, v20, s87, v209
	v_med3_f32 v20, v21, s87, v209
	v_cvt_pk_fp8_f32 v25, v19, v20 op_sel:[0,0,1]
	v_lshl_add_u64 v[16:17], v[16:17], 0, v[32:33]
	s_nop 15
	s_nop 15
	global_store_dwordx2 v[16:17], v[22:23], off nt
	global_store_dwordx2 v[16:17], v[24:25], off offset:128 nt
	v_pk_fma_f32 v[22:23], v[152:153], s[18:19], v[14:15] op_sel_hi:[1,0,1]
	v_mov_b32_e32 v24, v33
	v_med3_f32 v19, v22, s87, v209
	v_med3_f32 v25, v23, s87, v209
	v_pk_fma_f32 v[22:23], v[154:155], s[18:19], v[10:11] op_sel_hi:[1,0,1]
	v_cvt_pk_fp8_f32 v24, v19, v25
	v_med3_f32 v26, v22, s87, v209
	v_med3_f32 v27, v23, s87, v209
	v_pk_fma_f32 v[22:23], v[148:149], s[18:19], v[12:13] op_sel_hi:[1,0,1]
	v_mov_b32_e32 v25, v33
	v_med3_f32 v28, v22, s87, v209
	v_med3_f32 v29, v23, s87, v209
	v_cvt_pk_fp8_f32 v25, v28, v29
	v_pk_fma_f32 v[22:23], v[150:151], s[18:19], v[8:9] op_sel_hi:[1,0,1]
	v_cvt_pk_fp8_f32 v24, v26, v27 op_sel:[0,0,1]
	v_med3_f32 v19, v22, s87, v209
	v_med3_f32 v22, v23, s87, v209
	v_cvt_pk_fp8_f32 v25, v19, v22 op_sel:[0,0,1]
	v_pk_fma_f32 v[22:23], v[160:161], s[18:19], v[6:7] op_sel_hi:[1,0,1]
	v_mov_b32_e32 v26, v33
	v_med3_f32 v19, v22, s87, v209
	v_med3_f32 v27, v23, s87, v209
	v_pk_fma_f32 v[22:23], v[162:163], s[18:19], v[2:3] op_sel_hi:[1,0,1]
	v_cvt_pk_fp8_f32 v26, v19, v27
	v_med3_f32 v28, v22, s87, v209
	v_med3_f32 v29, v23, s87, v209
	v_pk_fma_f32 v[22:23], v[156:157], s[18:19], v[4:5] op_sel_hi:[1,0,1]
	v_mov_b32_e32 v27, v33
	v_med3_f32 v30, v22, s87, v209
	v_med3_f32 v31, v23, s87, v209
	v_cvt_pk_fp8_f32 v27, v30, v31
	v_or_b32_e32 v20, 16, v18
	v_pk_fma_f32 v[22:23], v[158:159], s[18:19], v[0:1] op_sel_hi:[1,0,1]
	v_ashrrev_i32_e32 v21, 31, v20
	v_med3_f32 v19, v22, s87, v209
	v_med3_f32 v22, v23, s87, v209
	v_lshlrev_b64 v[20:21], 11, v[20:21]
	v_cvt_pk_fp8_f32 v26, v28, v29 op_sel:[0,0,1]
	v_cvt_pk_fp8_f32 v27, v19, v22 op_sel:[0,0,1]
	v_lshl_add_u64 v[20:21], s[4:5], 0, v[20:21]
	v_lshl_add_u64 v[20:21], v[20:21], 0, v[32:33]
	v_pk_fma_f32 v[22:23], v[136:137], s[18:19], v[14:15] op_sel_hi:[1,0,1]
	global_store_dwordx2 v[20:21], v[24:25], off nt
	global_store_dwordx2 v[20:21], v[26:27], off offset:128 nt
	v_med3_f32 v19, v22, s87, v209
	v_med3_f32 v25, v23, s87, v209
	v_pk_fma_f32 v[22:23], v[138:139], s[18:19], v[10:11] op_sel_hi:[1,0,1]
	v_mov_b32_e32 v24, v33
	v_med3_f32 v26, v22, s87, v209
	v_med3_f32 v27, v23, s87, v209
	v_pk_fma_f32 v[22:23], v[132:133], s[18:19], v[12:13] op_sel_hi:[1,0,1]
	v_cvt_pk_fp8_f32 v24, v19, v25
	v_med3_f32 v28, v22, s87, v209
	v_med3_f32 v29, v23, s87, v209
	v_mov_b32_e32 v25, v33
	v_cvt_pk_fp8_f32 v25, v28, v29
	v_pk_fma_f32 v[22:23], v[134:135], s[18:19], v[8:9] op_sel_hi:[1,0,1]
	v_cvt_pk_fp8_f32 v24, v26, v27 op_sel:[0,0,1]
	v_med3_f32 v19, v22, s87, v209
	v_med3_f32 v22, v23, s87, v209
	v_cvt_pk_fp8_f32 v25, v19, v22 op_sel:[0,0,1]
	v_pk_fma_f32 v[22:23], v[144:145], s[18:19], v[6:7] op_sel_hi:[1,0,1]
	v_mov_b32_e32 v26, v33
	v_med3_f32 v19, v22, s87, v209
	v_med3_f32 v27, v23, s87, v209
	v_pk_fma_f32 v[22:23], v[146:147], s[18:19], v[2:3] op_sel_hi:[1,0,1]
	v_cvt_pk_fp8_f32 v26, v19, v27
	v_med3_f32 v28, v22, s87, v209
	v_med3_f32 v29, v23, s87, v209
	v_pk_fma_f32 v[22:23], v[140:141], s[18:19], v[4:5] op_sel_hi:[1,0,1]
	v_mov_b32_e32 v27, v33
	v_med3_f32 v30, v22, s87, v209
	v_med3_f32 v31, v23, s87, v209
	v_cvt_pk_fp8_f32 v27, v30, v31
	v_or_b32_e32 v20, 32, v18
	v_pk_fma_f32 v[22:23], v[142:143], s[18:19], v[0:1] op_sel_hi:[1,0,1]
	v_ashrrev_i32_e32 v21, 31, v20
	v_med3_f32 v19, v22, s87, v209
	v_med3_f32 v22, v23, s87, v209
	v_lshlrev_b64 v[20:21], 11, v[20:21]
	v_cvt_pk_fp8_f32 v26, v28, v29 op_sel:[0,0,1]
	v_cvt_pk_fp8_f32 v27, v19, v22 op_sel:[0,0,1]
	v_lshl_add_u64 v[20:21], s[4:5], 0, v[20:21]
	v_lshl_add_u64 v[20:21], v[20:21], 0, v[32:33]
	global_store_dwordx2 v[20:21], v[24:25], off nt
	global_store_dwordx2 v[20:21], v[26:27], off offset:128 nt
	v_pk_fma_f32 v[20:21], v[112:113], s[18:19], v[14:15] op_sel_hi:[1,0,1]
	v_mov_b32_e32 v22, v33
	v_med3_f32 v23, v20, s87, v209
	v_med3_f32 v24, v21, s87, v209
	v_pk_fma_f32 v[20:21], v[114:115], s[18:19], v[10:11] op_sel_hi:[1,0,1]
	v_cvt_pk_fp8_f32 v22, v23, v24
	v_med3_f32 v25, v20, s87, v209
	v_med3_f32 v26, v21, s87, v209
	v_pk_fma_f32 v[20:21], v[104:105], s[18:19], v[12:13] op_sel_hi:[1,0,1]
	v_mov_b32_e32 v23, v33
	v_med3_f32 v27, v20, s87, v209
	v_med3_f32 v28, v21, s87, v209
	v_cvt_pk_fp8_f32 v23, v27, v28
	v_pk_fma_f32 v[20:21], v[106:107], s[18:19], v[8:9] op_sel_hi:[1,0,1]
	v_cvt_pk_fp8_f32 v22, v25, v26 op_sel:[0,0,1]
	v_med3_f32 v20, v20, s87, v209
	v_med3_f32 v21, v21, s87, v209
	v_cvt_pk_fp8_f32 v23, v20, v21 op_sel:[0,0,1]
	v_pk_fma_f32 v[20:21], v[108:109], s[18:19], v[6:7] op_sel_hi:[1,0,1]
	v_mov_b32_e32 v24, v33
	v_med3_f32 v25, v20, s87, v209
	v_med3_f32 v26, v21, s87, v209
	v_pk_fma_f32 v[20:21], v[110:111], s[18:19], v[2:3] op_sel_hi:[1,0,1]
	v_cvt_pk_fp8_f32 v24, v25, v26
	v_med3_f32 v27, v20, s87, v209
	v_med3_f32 v28, v21, s87, v209
	v_pk_fma_f32 v[20:21], v[100:101], s[18:19], v[4:5] op_sel_hi:[1,0,1]
	v_mov_b32_e32 v25, v33
	v_med3_f32 v29, v20, s87, v209
	v_med3_f32 v30, v21, s87, v209
	v_cvt_pk_fp8_f32 v25, v29, v30
	v_or_b32_e32 v18, 48, v18
	v_pk_fma_f32 v[20:21], v[102:103], s[18:19], v[0:1] op_sel_hi:[1,0,1]
	v_ashrrev_i32_e32 v19, 31, v18
	v_med3_f32 v20, v20, s87, v209
	v_med3_f32 v21, v21, s87, v209
	v_lshlrev_b64 v[18:19], 11, v[18:19]
	v_cvt_pk_fp8_f32 v24, v27, v28 op_sel:[0,0,1]
	v_cvt_pk_fp8_f32 v25, v20, v21 op_sel:[0,0,1]
	v_lshl_add_u64 v[18:19], s[4:5], 0, v[18:19]
	v_lshl_add_u64 v[18:19], v[18:19], 0, v[32:33]
	v_pk_fma_f32 v[20:21], v[124:125], s[18:19], v[14:15] op_sel_hi:[1,0,1]
	global_store_dwordx2 v[18:19], v[22:23], off nt
	global_store_dwordx2 v[18:19], v[24:25], off offset:128 nt
	v_med3_f32 v23, v20, s87, v209
	v_med3_f32 v24, v21, s87, v209
	v_pk_fma_f32 v[20:21], v[126:127], s[18:19], v[10:11] op_sel_hi:[1,0,1]
	v_mov_b32_e32 v22, v33
	v_med3_f32 v25, v20, s87, v209
	v_med3_f32 v26, v21, s87, v209
	v_pk_fma_f32 v[20:21], v[116:117], s[18:19], v[12:13] op_sel_hi:[1,0,1]
	v_cvt_pk_fp8_f32 v22, v23, v24
	v_med3_f32 v27, v20, s87, v209
	v_med3_f32 v28, v21, s87, v209
	v_mov_b32_e32 v23, v33
	v_cvt_pk_fp8_f32 v23, v27, v28
	v_pk_fma_f32 v[20:21], v[118:119], s[18:19], v[8:9] op_sel_hi:[1,0,1]
	v_cvt_pk_fp8_f32 v22, v25, v26 op_sel:[0,0,1]
	v_med3_f32 v20, v20, s87, v209
	v_med3_f32 v21, v21, s87, v209
	v_cvt_pk_fp8_f32 v23, v20, v21 op_sel:[0,0,1]
	v_pk_fma_f32 v[20:21], v[128:129], s[18:19], v[6:7] op_sel_hi:[1,0,1]
	v_mov_b32_e32 v24, v33
	v_med3_f32 v25, v20, s87, v209
	v_med3_f32 v26, v21, s87, v209
	v_pk_fma_f32 v[20:21], v[130:131], s[18:19], v[2:3] op_sel_hi:[1,0,1]
	v_cvt_pk_fp8_f32 v24, v25, v26
	v_med3_f32 v27, v20, s87, v209
	v_med3_f32 v28, v21, s87, v209
	v_pk_fma_f32 v[20:21], v[120:121], s[18:19], v[4:5] op_sel_hi:[1,0,1]
	v_mov_b32_e32 v25, v33
	v_med3_f32 v29, v20, s87, v209
	v_med3_f32 v30, v21, s87, v209
	v_cvt_pk_fp8_f32 v25, v29, v30
	v_pk_fma_f32 v[20:21], v[122:123], s[18:19], v[0:1] op_sel_hi:[1,0,1]
	v_cvt_pk_fp8_f32 v24, v27, v28 op_sel:[0,0,1]
	v_med3_f32 v20, v20, s87, v209
	v_med3_f32 v21, v21, s87, v209
	v_cvt_pk_fp8_f32 v25, v20, v21 op_sel:[0,0,1]
	v_add_co_u32_e32 v20, vcc, s88, v16
	v_lshl_add_u64 v[18:19], v[16:17], 0, s[20:21]
	s_nop 0
	v_addc_co_u32_e32 v21, vcc, 0, v17, vcc
	global_store_dwordx2 v[20:21], v[22:23], off nt
	global_store_dwordx2 v[18:19], v[24:25], off offset:128 nt
	v_pk_fma_f32 v[20:21], v[96:97], s[18:19], v[14:15] op_sel_hi:[1,0,1]
	v_mov_b32_e32 v22, v33
	v_med3_f32 v23, v20, s87, v209
	v_med3_f32 v24, v21, s87, v209
	v_pk_fma_f32 v[20:21], v[98:99], s[18:19], v[10:11] op_sel_hi:[1,0,1]
	v_cvt_pk_fp8_f32 v22, v23, v24
	v_med3_f32 v25, v20, s87, v209
	v_med3_f32 v26, v21, s87, v209
	v_pk_fma_f32 v[20:21], v[88:89], s[18:19], v[12:13] op_sel_hi:[1,0,1]
	v_mov_b32_e32 v23, v33
	v_med3_f32 v27, v20, s87, v209
	v_med3_f32 v28, v21, s87, v209
	v_cvt_pk_fp8_f32 v23, v27, v28
	v_pk_fma_f32 v[20:21], v[90:91], s[18:19], v[8:9] op_sel_hi:[1,0,1]
	v_cvt_pk_fp8_f32 v22, v25, v26 op_sel:[0,0,1]
	v_med3_f32 v20, v20, s87, v209
	v_med3_f32 v21, v21, s87, v209
	v_cvt_pk_fp8_f32 v23, v20, v21 op_sel:[0,0,1]
	v_pk_fma_f32 v[20:21], v[92:93], s[18:19], v[6:7] op_sel_hi:[1,0,1]
	v_mov_b32_e32 v24, v33
	v_med3_f32 v25, v20, s87, v209
	v_med3_f32 v26, v21, s87, v209
	v_pk_fma_f32 v[20:21], v[94:95], s[18:19], v[2:3] op_sel_hi:[1,0,1]
	v_cvt_pk_fp8_f32 v24, v25, v26
	v_med3_f32 v27, v20, s87, v209
	v_med3_f32 v28, v21, s87, v209
	v_pk_fma_f32 v[20:21], v[84:85], s[18:19], v[4:5] op_sel_hi:[1,0,1]
	v_mov_b32_e32 v25, v33
	v_med3_f32 v29, v20, s87, v209
	v_med3_f32 v30, v21, s87, v209
	v_cvt_pk_fp8_f32 v25, v29, v30
	v_pk_fma_f32 v[20:21], v[86:87], s[18:19], v[0:1] op_sel_hi:[1,0,1]
	v_cvt_pk_fp8_f32 v24, v27, v28 op_sel:[0,0,1]
	v_med3_f32 v20, v20, s87, v209
	v_med3_f32 v21, v21, s87, v209
	v_cvt_pk_fp8_f32 v25, v20, v21 op_sel:[0,0,1]
	v_add_co_u32_e32 v20, vcc, s89, v16
	v_lshl_add_u64 v[18:19], v[16:17], 0, s[22:23]
	s_nop 0
	v_addc_co_u32_e32 v21, vcc, 0, v17, vcc
	global_store_dwordx2 v[20:21], v[22:23], off nt
	global_store_dwordx2 v[18:19], v[24:25], off offset:128 nt
	v_pk_fma_f32 v[20:21], v[80:81], s[18:19], v[14:15] op_sel_hi:[1,0,1]
	v_mov_b32_e32 v22, v33
	v_med3_f32 v23, v20, s87, v209
	v_med3_f32 v24, v21, s87, v209
	v_pk_fma_f32 v[20:21], v[82:83], s[18:19], v[10:11] op_sel_hi:[1,0,1]
	v_cvt_pk_fp8_f32 v22, v23, v24
	v_med3_f32 v25, v20, s87, v209
	v_med3_f32 v26, v21, s87, v209
	v_pk_fma_f32 v[20:21], v[76:77], s[18:19], v[12:13] op_sel_hi:[1,0,1]
	v_mov_b32_e32 v23, v33
	v_med3_f32 v27, v20, s87, v209
	v_med3_f32 v28, v21, s87, v209
	v_cvt_pk_fp8_f32 v23, v27, v28
	v_pk_fma_f32 v[20:21], v[78:79], s[18:19], v[8:9] op_sel_hi:[1,0,1]
	v_cvt_pk_fp8_f32 v22, v25, v26 op_sel:[0,0,1]
	v_med3_f32 v20, v20, s87, v209
	v_med3_f32 v21, v21, s87, v209
	v_cvt_pk_fp8_f32 v23, v20, v21 op_sel:[0,0,1]
	v_pk_fma_f32 v[20:21], v[72:73], s[18:19], v[6:7] op_sel_hi:[1,0,1]
	v_mov_b32_e32 v24, v33
	v_med3_f32 v25, v20, s87, v209
	v_med3_f32 v26, v21, s87, v209
	v_pk_fma_f32 v[20:21], v[74:75], s[18:19], v[2:3] op_sel_hi:[1,0,1]
	v_cvt_pk_fp8_f32 v24, v25, v26
	v_med3_f32 v27, v20, s87, v209
	v_med3_f32 v28, v21, s87, v209
	v_pk_fma_f32 v[20:21], v[68:69], s[18:19], v[4:5] op_sel_hi:[1,0,1]
	v_mov_b32_e32 v25, v33
	v_med3_f32 v29, v20, s87, v209
	v_med3_f32 v30, v21, s87, v209
	v_cvt_pk_fp8_f32 v25, v29, v30
	v_pk_fma_f32 v[20:21], v[70:71], s[18:19], v[0:1] op_sel_hi:[1,0,1]
	v_cvt_pk_fp8_f32 v24, v27, v28 op_sel:[0,0,1]
	v_med3_f32 v20, v20, s87, v209
	v_med3_f32 v21, v21, s87, v209
	v_cvt_pk_fp8_f32 v25, v20, v21 op_sel:[0,0,1]
	v_add_co_u32_e32 v20, vcc, s90, v16
	v_pk_fma_f32 v[10:11], v[66:67], s[18:19], v[10:11] op_sel_hi:[1,0,1]
	s_nop 0
	v_addc_co_u32_e32 v21, vcc, 0, v17, vcc
	v_lshl_add_u64 v[18:19], v[16:17], 0, s[24:25]
	global_store_dwordx2 v[20:21], v[22:23], off nt
	global_store_dwordx2 v[18:19], v[24:25], off offset:128 nt
	v_med3_f32 v20, v10, s87, v209
	v_med3_f32 v21, v11, s87, v209
	v_pk_fma_f32 v[10:11], v[60:61], s[18:19], v[12:13] op_sel_hi:[1,0,1]
	v_pk_fma_f32 v[8:9], v[62:63], s[18:19], v[8:9] op_sel_hi:[1,0,1]
	v_med3_f32 v12, v10, s87, v209
	v_med3_f32 v13, v11, s87, v209
	v_mov_b32_e32 v11, v33
	v_cvt_pk_fp8_f32 v11, v12, v13
	v_med3_f32 v8, v8, s87, v209
	v_med3_f32 v9, v9, s87, v209
	v_pk_fma_f32 v[2:3], v[58:59], s[18:19], v[2:3] op_sel_hi:[1,0,1]
	v_pk_fma_f32 v[14:15], v[64:65], s[18:19], v[14:15] op_sel_hi:[1,0,1]
	v_cvt_pk_fp8_f32 v11, v8, v9 op_sel:[0,0,1]
	v_pk_fma_f32 v[6:7], v[56:57], s[18:19], v[6:7] op_sel_hi:[1,0,1]
	v_med3_f32 v8, v2, s87, v209
	v_med3_f32 v9, v3, s87, v209
	v_pk_fma_f32 v[2:3], v[52:53], s[18:19], v[4:5] op_sel_hi:[1,0,1]
	v_med3_f32 v14, v14, s87, v209
	v_med3_f32 v15, v15, s87, v209
	v_mov_b32_e32 v10, v33
	v_med3_f32 v6, v6, s87, v209
	v_med3_f32 v7, v7, s87, v209
	v_med3_f32 v4, v2, s87, v209
	v_med3_f32 v5, v3, s87, v209
	v_mov_b32_e32 v2, v33
	v_mov_b32_e32 v3, v33
	v_cvt_pk_fp8_f32 v10, v14, v15
	v_cvt_pk_fp8_f32 v2, v6, v7
	v_cvt_pk_fp8_f32 v3, v4, v5
	v_pk_fma_f32 v[0:1], v[54:55], s[18:19], v[0:1] op_sel_hi:[1,0,1]
	v_cvt_pk_fp8_f32 v10, v20, v21 op_sel:[0,0,1]
	v_med3_f32 v0, v0, s87, v209
	v_med3_f32 v1, v1, s87, v209
	v_cvt_pk_fp8_f32 v2, v8, v9 op_sel:[0,0,1]
	v_cvt_pk_fp8_f32 v3, v0, v1 op_sel:[0,0,1]
	v_add_co_u32_e32 v0, vcc, s91, v16
	v_readlane_b32 s82, v254, 53
	s_nop 0
	v_addc_co_u32_e32 v1, vcc, 0, v17, vcc
	v_lshl_add_u64 v[18:19], v[16:17], 0, s[26:27]
	s_and_b64 vcc, exec, s[2:3]
	s_mov_b32 s80, s78
	v_readlane_b32 s83, v254, 54
	global_store_dwordx2 v[0:1], v[10:11], off nt
	global_store_dwordx2 v[18:19], v[2:3], off offset:128 nt
	s_cbranch_vccnz .LBB0_1676
	s_andn2_b64 vcc, exec, s[10:11]
	s_cbranch_vccnz .LBB0_1659
	s_barrier
	s_branch .LBB0_1659
